# non-temporal on the merge GEMM's gate loads and the final norm's loads and output stores
# baseline (speedup 1.0000x reference)
.LBB0_861:
	v_mov_b32_e32 v132, v184
	v_mov_b32_e32 v130, v183
	global_load_dwordx4 v[148:151], v130, s[16:17] offset:3584 nt
	s_lshl_b64 s[14:15], s[18:19], 11
	s_add_u32 s9, s44, s14
	s_addc_u32 s18, s45, s15
	s_lshl_b64 s[14:15], s[62:63], 1
	s_add_u32 s14, s9, s14
	s_addc_u32 s15, s18, s15
	v_lshl_add_u64 v[146:147], s[16:17], 0, v[130:131]
	v_mov_b32_e32 v133, v131
	s_mov_b32 s9, 0x1e000
	v_lshl_add_u64 v[144:145], v[132:133], 1, s[14:15]
	v_add_co_u32_e32 v132, vcc, s9, v146
	s_mov_b32 s9, 0x3c000
	s_nop 0
	v_addc_co_u32_e32 v133, vcc, 0, v147, vcc
	global_load_dwordx4 v[140:143], v[132:133], off offset:3584 nt
	v_add_co_u32_e32 v132, vcc, s9, v146
	s_mov_b32 s9, 0x5a000
	s_nop 0
	v_addc_co_u32_e32 v133, vcc, 0, v147, vcc
	global_load_dwordx4 v[136:139], v[132:133], off offset:3584 nt
	v_add_co_u32_e32 v132, vcc, s9, v146
	s_mov_b32 s9, 0x8000
	s_nop 0
	v_addc_co_u32_e32 v133, vcc, 0, v147, vcc
	global_load_dwordx4 v[132:135], v[132:133], off offset:3584 nt
	s_mov_b32 s16, s8
	s_mov_b32 s17, s51
	s_mov_b64 s[64:65], s[12:13]
	s_mov_b64 s[14:15], s[10:11]
	s_mov_b32 s53, 0x42b17218
	s_waitcnt vmcnt(0)
	v_cvt_pk_f32_fp8_e32 v[152:153], v148
	v_cvt_pk_f32_fp8_e32 v[156:157], v149
	v_cvt_pk_f32_fp8_sdwa v[154:155], v148 src0_sel:WORD_1
	v_cvt_pk_f32_fp8_sdwa v[148:149], v149 src0_sel:WORD_1
	v_add_f32_e32 v130, 1.0, v152
	v_rcp_f32_e32 v152, v130
	v_add_f32_e32 v130, 1.0, v156
	v_rcp_f32_e32 v156, v130
	v_add_f32_e32 v130, 1.0, v153
	v_rcp_f32_e32 v153, v130
	v_add_f32_e32 v130, 1.0, v157
	v_rcp_f32_e32 v157, v130
	v_pk_mul_f32 v[126:127], v[126:127], v[152:153]
	v_pk_mul_f32 v[152:153], v[122:123], v[156:157]
	v_add_f32_e32 v123, 1.0, v148
	v_add_f32_e32 v122, 1.0, v154
	v_rcp_f32_e32 v148, v123
	v_add_f32_e32 v123, 1.0, v155
	v_rcp_f32_e32 v122, v122
	v_rcp_f32_e32 v123, v123
	s_nop 0
	v_pk_mul_f32 v[128:129], v[128:129], v[122:123]
	v_add_f32_e32 v122, 1.0, v149
	v_rcp_f32_e32 v149, v122
	v_cvt_pk_bf16_f32 v122, v126, v127
	v_cvt_pk_bf16_f32 v123, v128, v129
	v_cvt_pk_f32_fp8_e32 v[126:127], v151
	v_pk_mul_f32 v[148:149], v[124:125], v[148:149]
	v_cvt_pk_bf16_f32 v124, v152, v153
	v_cvt_pk_bf16_f32 v125, v148, v149
	global_store_dwordx4 v[144:145], v[122:125], off
	v_add_f32_e32 v126, 1.0, v126
	v_cvt_pk_f32_fp8_sdwa v[128:129], v151 src0_sel:WORD_1
	v_cvt_pk_f32_fp8_e32 v[122:123], v150
	v_rcp_f32_e32 v126, v126
	v_cvt_pk_f32_fp8_sdwa v[124:125], v150 src0_sel:WORD_1
	v_add_f32_e32 v122, 1.0, v122
	v_add_f32_e32 v123, 1.0, v123
	v_rcp_f32_e32 v122, v122
	v_rcp_f32_e32 v123, v123
	s_nop 0
	v_pk_mul_f32 v[118:119], v[118:119], v[122:123]
	v_add_f32_e32 v122, 1.0, v127
	v_rcp_f32_e32 v127, v122
	s_nop 0
	v_pk_mul_f32 v[122:123], v[114:115], v[126:127]
	v_add_f32_e32 v115, 1.0, v128
	v_add_f32_e32 v114, 1.0, v124
	v_rcp_f32_e32 v124, v115
	v_add_f32_e32 v115, 1.0, v125
	v_rcp_f32_e32 v114, v114
	v_rcp_f32_e32 v115, v115
	s_nop 0
	v_pk_mul_f32 v[120:121], v[120:121], v[114:115]
	v_add_f32_e32 v114, 1.0, v129
	v_rcp_f32_e32 v125, v114
	v_cvt_pk_bf16_f32 v114, v118, v119
	v_cvt_pk_bf16_f32 v115, v120, v121
	v_cvt_pk_f32_fp8_e32 v[118:119], v141
	v_pk_mul_f32 v[124:125], v[116:117], v[124:125]
	v_cvt_pk_bf16_f32 v116, v122, v123
	v_cvt_pk_bf16_f32 v117, v124, v125
	global_store_dwordx4 v[144:145], v[114:117], off offset:16
	v_add_f32_e32 v118, 1.0, v118
	v_cvt_pk_f32_fp8_sdwa v[120:121], v141 src0_sel:WORD_1
	v_cvt_pk_f32_fp8_e32 v[114:115], v140
	v_rcp_f32_e32 v118, v118
	v_cvt_pk_f32_fp8_sdwa v[116:117], v140 src0_sel:WORD_1
	v_add_f32_e32 v114, 1.0, v114
	v_add_f32_e32 v115, 1.0, v115
	v_rcp_f32_e32 v114, v114
	v_rcp_f32_e32 v115, v115
	s_nop 0
	v_pk_mul_f32 v[110:111], v[110:111], v[114:115]
	v_add_f32_e32 v114, 1.0, v119
	v_rcp_f32_e32 v119, v114
	s_nop 0
	v_pk_mul_f32 v[114:115], v[106:107], v[118:119]
	v_add_f32_e32 v107, 1.0, v120
	v_add_f32_e32 v106, 1.0, v116
	v_rcp_f32_e32 v116, v107
	v_add_f32_e32 v107, 1.0, v117
	v_rcp_f32_e32 v106, v106
	v_rcp_f32_e32 v107, v107
	s_nop 0
	v_pk_mul_f32 v[112:113], v[112:113], v[106:107]
	v_add_f32_e32 v106, 1.0, v121
	v_rcp_f32_e32 v117, v106
	v_cvt_pk_bf16_f32 v106, v110, v111
	v_add_co_u32_e32 v110, vcc, s9, v144
	v_pk_mul_f32 v[116:117], v[108:109], v[116:117]
	v_cvt_pk_bf16_f32 v107, v112, v113
	v_cvt_pk_bf16_f32 v108, v114, v115
	v_cvt_pk_bf16_f32 v109, v116, v117
	v_addc_co_u32_e32 v111, vcc, 0, v145, vcc
	global_store_dwordx4 v[110:111], v[106:109], off
	v_cvt_pk_f32_fp8_e32 v[112:113], v143
	v_cvt_pk_f32_fp8_sdwa v[114:115], v143 src0_sel:WORD_1
	v_cvt_pk_f32_fp8_e32 v[106:107], v142
	v_cvt_pk_f32_fp8_sdwa v[108:109], v142 src0_sel:WORD_1
	v_add_f32_e32 v112, 1.0, v112
	v_rcp_f32_e32 v112, v112
	v_add_f32_e32 v106, 1.0, v106
	v_add_f32_e32 v107, 1.0, v107
	v_rcp_f32_e32 v106, v106
	v_rcp_f32_e32 v107, v107
	s_mov_b32 s9, 0x10000
	v_pk_mul_f32 v[102:103], v[102:103], v[106:107]
	v_add_f32_e32 v106, 1.0, v113
	v_rcp_f32_e32 v113, v106
	s_nop 0
	v_pk_mul_f32 v[106:107], v[98:99], v[112:113]
	v_add_f32_e32 v99, 1.0, v114
	v_add_f32_e32 v98, 1.0, v108
	v_rcp_f32_e32 v108, v99
	v_add_f32_e32 v99, 1.0, v109
	v_rcp_f32_e32 v98, v98
	v_rcp_f32_e32 v99, v99
	s_nop 0
	v_pk_mul_f32 v[104:105], v[104:105], v[98:99]
	v_add_f32_e32 v98, 1.0, v115
	v_rcp_f32_e32 v109, v98
	v_cvt_pk_bf16_f32 v98, v102, v103
	v_cvt_pk_bf16_f32 v99, v104, v105
	v_cvt_pk_f32_fp8_e32 v[102:103], v137
	v_pk_mul_f32 v[108:109], v[100:101], v[108:109]
	v_cvt_pk_bf16_f32 v100, v106, v107
	v_cvt_pk_bf16_f32 v101, v108, v109
	global_store_dwordx4 v[110:111], v[98:101], off offset:16
	v_add_f32_e32 v102, 1.0, v102
	v_cvt_pk_f32_fp8_sdwa v[104:105], v137 src0_sel:WORD_1
	v_cvt_pk_f32_fp8_e32 v[98:99], v136
	v_rcp_f32_e32 v102, v102
	v_cvt_pk_f32_fp8_sdwa v[100:101], v136 src0_sel:WORD_1
	v_add_f32_e32 v98, 1.0, v98
	v_add_f32_e32 v99, 1.0, v99
	v_rcp_f32_e32 v98, v98
	v_rcp_f32_e32 v99, v99
	s_nop 0
	v_pk_mul_f32 v[94:95], v[94:95], v[98:99]
	v_add_f32_e32 v98, 1.0, v103
	v_rcp_f32_e32 v103, v98
	s_nop 0
	v_pk_mul_f32 v[98:99], v[90:91], v[102:103]
	v_add_f32_e32 v91, 1.0, v104
	v_add_f32_e32 v90, 1.0, v100
	v_rcp_f32_e32 v100, v91
	v_add_f32_e32 v91, 1.0, v101
	v_rcp_f32_e32 v90, v90
	v_rcp_f32_e32 v91, v91
	s_nop 0
	v_pk_mul_f32 v[96:97], v[96:97], v[90:91]
	v_add_f32_e32 v90, 1.0, v105
	v_rcp_f32_e32 v101, v90
	v_cvt_pk_bf16_f32 v90, v94, v95
	v_add_co_u32_e32 v94, vcc, s9, v144
	v_pk_mul_f32 v[100:101], v[92:93], v[100:101]
	v_cvt_pk_bf16_f32 v91, v96, v97
	v_cvt_pk_bf16_f32 v92, v98, v99
	v_cvt_pk_bf16_f32 v93, v100, v101
	v_addc_co_u32_e32 v95, vcc, 0, v145, vcc
	global_store_dwordx4 v[94:95], v[90:93], off
	v_cvt_pk_f32_fp8_e32 v[96:97], v139
	v_cvt_pk_f32_fp8_sdwa v[98:99], v139 src0_sel:WORD_1
	v_cvt_pk_f32_fp8_e32 v[90:91], v138
	v_cvt_pk_f32_fp8_sdwa v[92:93], v138 src0_sel:WORD_1
	v_add_f32_e32 v96, 1.0, v96
	v_rcp_f32_e32 v96, v96
	v_add_f32_e32 v90, 1.0, v90
	v_add_f32_e32 v91, 1.0, v91
	v_rcp_f32_e32 v90, v90
	v_rcp_f32_e32 v91, v91
	s_mov_b32 s9, 0x18000
	v_pk_mul_f32 v[86:87], v[86:87], v[90:91]
	v_add_f32_e32 v90, 1.0, v97
	v_rcp_f32_e32 v97, v90
	s_nop 0
	v_pk_mul_f32 v[90:91], v[82:83], v[96:97]
	v_add_f32_e32 v83, 1.0, v98
	v_add_f32_e32 v82, 1.0, v92
	v_rcp_f32_e32 v92, v83
	v_add_f32_e32 v83, 1.0, v93
	v_rcp_f32_e32 v82, v82
	v_rcp_f32_e32 v83, v83
	s_nop 0
	v_pk_mul_f32 v[88:89], v[88:89], v[82:83]
	v_add_f32_e32 v82, 1.0, v99
	v_rcp_f32_e32 v93, v82
	v_cvt_pk_bf16_f32 v82, v86, v87
	v_cvt_pk_bf16_f32 v83, v88, v89
	v_cvt_pk_f32_fp8_e32 v[86:87], v133
	v_pk_mul_f32 v[92:93], v[84:85], v[92:93]
	v_cvt_pk_bf16_f32 v84, v90, v91
	v_cvt_pk_bf16_f32 v85, v92, v93
	global_store_dwordx4 v[94:95], v[82:85], off offset:16
	v_add_f32_e32 v86, 1.0, v86
	v_cvt_pk_f32_fp8_sdwa v[88:89], v133 src0_sel:WORD_1
	v_cvt_pk_f32_fp8_e32 v[82:83], v132
	v_rcp_f32_e32 v86, v86
	v_cvt_pk_f32_fp8_sdwa v[84:85], v132 src0_sel:WORD_1
	v_add_f32_e32 v82, 1.0, v82
	v_add_f32_e32 v83, 1.0, v83
	v_rcp_f32_e32 v82, v82
	v_rcp_f32_e32 v83, v83
	s_nop 0
	v_pk_mul_f32 v[78:79], v[78:79], v[82:83]
	v_add_f32_e32 v82, 1.0, v87
	v_rcp_f32_e32 v87, v82
	s_nop 0
	v_pk_mul_f32 v[82:83], v[74:75], v[86:87]
	v_add_f32_e32 v75, 1.0, v88
	v_add_f32_e32 v74, 1.0, v84
	v_rcp_f32_e32 v84, v75
	v_add_f32_e32 v75, 1.0, v85
	v_rcp_f32_e32 v74, v74
	v_rcp_f32_e32 v75, v75
	s_nop 0
	v_pk_mul_f32 v[80:81], v[80:81], v[74:75]
	v_add_f32_e32 v74, 1.0, v89
	v_rcp_f32_e32 v85, v74
	v_cvt_pk_bf16_f32 v74, v78, v79
	v_add_co_u32_e32 v78, vcc, s9, v144
	v_pk_mul_f32 v[84:85], v[76:77], v[84:85]
	v_cvt_pk_bf16_f32 v75, v80, v81
	v_cvt_pk_bf16_f32 v76, v82, v83
	v_cvt_pk_bf16_f32 v77, v84, v85
	v_addc_co_u32_e32 v79, vcc, 0, v145, vcc
	global_store_dwordx4 v[78:79], v[74:77], off
	v_cvt_pk_f32_fp8_e32 v[80:81], v135
	v_cvt_pk_f32_fp8_sdwa v[82:83], v135 src0_sel:WORD_1
	v_cvt_pk_f32_fp8_e32 v[74:75], v134
	v_cvt_pk_f32_fp8_sdwa v[76:77], v134 src0_sel:WORD_1
	v_add_f32_e32 v80, 1.0, v80
	v_rcp_f32_e32 v80, v80
	v_add_f32_e32 v74, 1.0, v74
	v_add_f32_e32 v75, 1.0, v75
	v_rcp_f32_e32 v74, v74
	v_rcp_f32_e32 v75, v75
	s_mov_b32 s9, 0xf0000
	v_pk_mul_f32 v[70:71], v[70:71], v[74:75]
	v_add_f32_e32 v74, 1.0, v81
	v_rcp_f32_e32 v81, v74
	s_nop 0
	v_pk_mul_f32 v[74:75], v[66:67], v[80:81]
	v_add_f32_e32 v67, 1.0, v82
	v_add_f32_e32 v66, 1.0, v76
	v_rcp_f32_e32 v76, v67
	v_add_f32_e32 v67, 1.0, v77
	v_rcp_f32_e32 v66, v66
	v_rcp_f32_e32 v67, v67
	s_nop 0
	v_pk_mul_f32 v[72:73], v[72:73], v[66:67]
	v_add_f32_e32 v66, 1.0, v83
	v_rcp_f32_e32 v77, v66
	v_cvt_pk_bf16_f32 v66, v70, v71
	v_cvt_pk_bf16_f32 v67, v72, v73
	v_pk_mul_f32 v[76:77], v[68:69], v[76:77]
	v_cvt_pk_bf16_f32 v68, v74, v75
	v_cvt_pk_bf16_f32 v69, v76, v77
	global_store_dwordx4 v[78:79], v[66:69], off offset:16
	s_nop 1
	v_add_co_u32_e32 v66, vcc, s9, v146
	s_mov_b32 s9, 0x10e000
	s_nop 0
	v_addc_co_u32_e32 v67, vcc, 0, v147, vcc
	global_load_dwordx4 v[74:77], v[66:67], off offset:3584 nt
	v_add_co_u32_e32 v66, vcc, s9, v146
	s_mov_b32 s9, 0x12c000
	s_nop 0
	v_addc_co_u32_e32 v67, vcc, 0, v147, vcc
	global_load_dwordx4 v[78:81], v[66:67], off offset:3584 nt
	v_add_co_u32_e32 v66, vcc, s9, v146
	s_mov_b32 s9, 0x14a000
	s_nop 0
	v_addc_co_u32_e32 v67, vcc, 0, v147, vcc
	global_load_dwordx4 v[70:73], v[66:67], off offset:3584 nt
	v_add_co_u32_e32 v66, vcc, s9, v146
	s_mov_b32 s9, 0x40000
	s_nop 0
	v_addc_co_u32_e32 v67, vcc, 0, v147, vcc
	global_load_dwordx4 v[66:69], v[66:67], off offset:3584 nt
	s_waitcnt vmcnt(0)
	v_cvt_pk_f32_fp8_e32 v[82:83], v74
	v_cvt_pk_f32_fp8_e32 v[86:87], v75
	v_cvt_pk_f32_fp8_sdwa v[84:85], v74 src0_sel:WORD_1
	v_cvt_pk_f32_fp8_sdwa v[74:75], v75 src0_sel:WORD_1
	v_add_f32_e32 v82, 1.0, v82
	v_add_f32_e32 v83, 1.0, v83
	v_rcp_f32_e32 v82, v82
	v_rcp_f32_e32 v83, v83
	v_add_f32_e32 v86, 1.0, v86
	v_rcp_f32_e32 v86, v86
	v_pk_mul_f32 v[62:63], v[62:63], v[82:83]
	v_add_f32_e32 v82, 1.0, v87
	v_rcp_f32_e32 v87, v82
	s_nop 0
	v_pk_mul_f32 v[82:83], v[58:59], v[86:87]
	v_add_f32_e32 v59, 1.0, v74
	v_add_f32_e32 v58, 1.0, v84
	v_rcp_f32_e32 v74, v59
	v_add_f32_e32 v59, 1.0, v85
	v_rcp_f32_e32 v58, v58
	v_rcp_f32_e32 v59, v59
	s_nop 0
	v_pk_mul_f32 v[64:65], v[64:65], v[58:59]
	v_add_f32_e32 v58, 1.0, v75
	v_rcp_f32_e32 v75, v58
	v_cvt_pk_bf16_f32 v58, v62, v63
	v_add_co_u32_e32 v62, vcc, s9, v144
	v_pk_mul_f32 v[74:75], v[60:61], v[74:75]
	v_cvt_pk_bf16_f32 v59, v64, v65
	v_cvt_pk_bf16_f32 v60, v82, v83
	v_cvt_pk_bf16_f32 v61, v74, v75
	v_addc_co_u32_e32 v63, vcc, 0, v145, vcc
	global_store_dwordx4 v[62:63], v[58:61], off
	v_cvt_pk_f32_fp8_e32 v[64:65], v77
	v_cvt_pk_f32_fp8_sdwa v[74:75], v77 src0_sel:WORD_1
	v_cvt_pk_f32_fp8_e32 v[58:59], v76
	v_cvt_pk_f32_fp8_sdwa v[60:61], v76 src0_sel:WORD_1
	v_add_f32_e32 v64, 1.0, v64
	v_rcp_f32_e32 v64, v64
	v_add_f32_e32 v58, 1.0, v58
	v_add_f32_e32 v59, 1.0, v59
	v_rcp_f32_e32 v58, v58
	v_rcp_f32_e32 v59, v59
	s_mov_b32 s9, 0x48000
	v_pk_mul_f32 v[54:55], v[54:55], v[58:59]
	v_add_f32_e32 v58, 1.0, v65
	v_rcp_f32_e32 v65, v58
	s_nop 0
	v_pk_mul_f32 v[58:59], v[50:51], v[64:65]
	v_add_f32_e32 v51, 1.0, v74
	v_add_f32_e32 v50, 1.0, v60
	v_rcp_f32_e32 v60, v51
	v_add_f32_e32 v51, 1.0, v61
	v_rcp_f32_e32 v50, v50
	v_rcp_f32_e32 v51, v51
	s_nop 0
	v_pk_mul_f32 v[56:57], v[56:57], v[50:51]
	v_add_f32_e32 v50, 1.0, v75
	v_rcp_f32_e32 v61, v50
	v_cvt_pk_bf16_f32 v50, v54, v55
	v_cvt_pk_bf16_f32 v51, v56, v57
	v_cvt_pk_f32_fp8_e32 v[54:55], v79
	v_pk_mul_f32 v[60:61], v[52:53], v[60:61]
	v_cvt_pk_bf16_f32 v52, v58, v59
	v_cvt_pk_bf16_f32 v53, v60, v61
	global_store_dwordx4 v[62:63], v[50:53], off offset:16
	v_add_f32_e32 v54, 1.0, v54
	v_cvt_pk_f32_fp8_sdwa v[56:57], v79 src0_sel:WORD_1
	v_cvt_pk_f32_fp8_e32 v[50:51], v78
	v_rcp_f32_e32 v54, v54
	v_cvt_pk_f32_fp8_sdwa v[52:53], v78 src0_sel:WORD_1
	v_add_f32_e32 v50, 1.0, v50
	v_add_f32_e32 v51, 1.0, v51
	v_rcp_f32_e32 v50, v50
	v_rcp_f32_e32 v51, v51
	s_nop 0
	v_pk_mul_f32 v[46:47], v[46:47], v[50:51]
	v_add_f32_e32 v50, 1.0, v55
	v_rcp_f32_e32 v55, v50
	s_nop 0
	v_pk_mul_f32 v[50:51], v[42:43], v[54:55]
	v_add_f32_e32 v43, 1.0, v56
	v_add_f32_e32 v42, 1.0, v52
	v_rcp_f32_e32 v52, v43
	v_add_f32_e32 v43, 1.0, v53
	v_rcp_f32_e32 v42, v42
	v_rcp_f32_e32 v43, v43
	s_nop 0
	v_pk_mul_f32 v[48:49], v[48:49], v[42:43]
	v_add_f32_e32 v42, 1.0, v57
	v_rcp_f32_e32 v53, v42
	v_cvt_pk_bf16_f32 v42, v46, v47
	v_add_co_u32_e32 v46, vcc, s9, v144
	v_pk_mul_f32 v[52:53], v[44:45], v[52:53]
	v_cvt_pk_bf16_f32 v43, v48, v49
	v_cvt_pk_bf16_f32 v44, v50, v51
	v_cvt_pk_bf16_f32 v45, v52, v53
	v_addc_co_u32_e32 v47, vcc, 0, v145, vcc
	global_store_dwordx4 v[46:47], v[42:45], off
	v_cvt_pk_f32_fp8_e32 v[48:49], v81
	v_cvt_pk_f32_fp8_sdwa v[50:51], v81 src0_sel:WORD_1
	v_cvt_pk_f32_fp8_e32 v[42:43], v80
	v_cvt_pk_f32_fp8_sdwa v[44:45], v80 src0_sel:WORD_1
	v_add_f32_e32 v48, 1.0, v48
	v_rcp_f32_e32 v48, v48
	v_add_f32_e32 v42, 1.0, v42
	v_add_f32_e32 v43, 1.0, v43
	v_rcp_f32_e32 v42, v42
	v_rcp_f32_e32 v43, v43
	s_mov_b32 s9, 0x50000
	v_pk_mul_f32 v[38:39], v[38:39], v[42:43]
	v_add_f32_e32 v42, 1.0, v49
	v_rcp_f32_e32 v49, v42
	s_nop 0
	v_pk_mul_f32 v[42:43], v[34:35], v[48:49]
	v_add_f32_e32 v35, 1.0, v50
	v_add_f32_e32 v34, 1.0, v44
	v_rcp_f32_e32 v44, v35
	v_add_f32_e32 v35, 1.0, v45
	v_rcp_f32_e32 v34, v34
	v_rcp_f32_e32 v35, v35
	s_nop 0
	v_pk_mul_f32 v[40:41], v[40:41], v[34:35]
	v_add_f32_e32 v34, 1.0, v51
	v_rcp_f32_e32 v45, v34
	v_cvt_pk_bf16_f32 v34, v38, v39
	v_cvt_pk_bf16_f32 v35, v40, v41
	v_cvt_pk_f32_fp8_e32 v[38:39], v71
	v_pk_mul_f32 v[44:45], v[36:37], v[44:45]
	v_cvt_pk_bf16_f32 v36, v42, v43
	v_cvt_pk_bf16_f32 v37, v44, v45
	global_store_dwordx4 v[46:47], v[34:37], off offset:16
	v_add_f32_e32 v38, 1.0, v38
	v_cvt_pk_f32_fp8_sdwa v[40:41], v71 src0_sel:WORD_1
	v_cvt_pk_f32_fp8_e32 v[34:35], v70
	v_rcp_f32_e32 v38, v38
	v_cvt_pk_f32_fp8_sdwa v[36:37], v70 src0_sel:WORD_1
	v_add_f32_e32 v34, 1.0, v34
	v_add_f32_e32 v35, 1.0, v35
	v_rcp_f32_e32 v34, v34
	v_rcp_f32_e32 v35, v35
	s_nop 0
	v_pk_mul_f32 v[30:31], v[30:31], v[34:35]
	v_add_f32_e32 v34, 1.0, v39
	v_rcp_f32_e32 v39, v34
	s_nop 0
	v_pk_mul_f32 v[34:35], v[26:27], v[38:39]
	v_add_f32_e32 v27, 1.0, v40
	v_add_f32_e32 v26, 1.0, v36
	v_rcp_f32_e32 v36, v27
	v_add_f32_e32 v27, 1.0, v37
	v_rcp_f32_e32 v26, v26
	v_rcp_f32_e32 v27, v27
	s_nop 0
	v_pk_mul_f32 v[32:33], v[32:33], v[26:27]
	v_add_f32_e32 v26, 1.0, v41
	v_rcp_f32_e32 v37, v26
	v_cvt_pk_bf16_f32 v26, v30, v31
	v_add_co_u32_e32 v30, vcc, s9, v144
	v_pk_mul_f32 v[36:37], v[28:29], v[36:37]
	v_cvt_pk_bf16_f32 v27, v32, v33
	v_cvt_pk_bf16_f32 v28, v34, v35
	v_cvt_pk_bf16_f32 v29, v36, v37
	v_addc_co_u32_e32 v31, vcc, 0, v145, vcc
	global_store_dwordx4 v[30:31], v[26:29], off
	v_cvt_pk_f32_fp8_e32 v[32:33], v73
	v_cvt_pk_f32_fp8_sdwa v[34:35], v73 src0_sel:WORD_1
	v_cvt_pk_f32_fp8_e32 v[26:27], v72
	v_cvt_pk_f32_fp8_sdwa v[28:29], v72 src0_sel:WORD_1
	v_add_f32_e32 v32, 1.0, v32
	v_rcp_f32_e32 v32, v32
	v_add_f32_e32 v26, 1.0, v26
	v_add_f32_e32 v27, 1.0, v27
	v_rcp_f32_e32 v26, v26
	v_rcp_f32_e32 v27, v27
	s_mov_b32 s9, 0x58000
	v_pk_mul_f32 v[22:23], v[22:23], v[26:27]
	v_add_f32_e32 v26, 1.0, v33
	v_rcp_f32_e32 v33, v26
	s_nop 0
	v_pk_mul_f32 v[26:27], v[18:19], v[32:33]
	v_add_f32_e32 v19, 1.0, v34
	v_add_f32_e32 v18, 1.0, v28
	v_rcp_f32_e32 v28, v19
	v_add_f32_e32 v19, 1.0, v29
	v_rcp_f32_e32 v18, v18
	v_rcp_f32_e32 v19, v19
	s_nop 0
	v_pk_mul_f32 v[24:25], v[24:25], v[18:19]
	v_add_f32_e32 v18, 1.0, v35
	v_rcp_f32_e32 v29, v18
	v_cvt_pk_bf16_f32 v18, v22, v23
	v_cvt_pk_bf16_f32 v19, v24, v25
	v_cvt_pk_f32_fp8_e32 v[22:23], v67
	v_pk_mul_f32 v[28:29], v[20:21], v[28:29]
	v_cvt_pk_bf16_f32 v20, v26, v27
	v_cvt_pk_bf16_f32 v21, v28, v29
	global_store_dwordx4 v[30:31], v[18:21], off offset:16
	v_add_f32_e32 v22, 1.0, v22
	v_cvt_pk_f32_fp8_sdwa v[24:25], v67 src0_sel:WORD_1
	v_cvt_pk_f32_fp8_e32 v[18:19], v66
	v_rcp_f32_e32 v22, v22
	v_cvt_pk_f32_fp8_sdwa v[20:21], v66 src0_sel:WORD_1
	v_add_f32_e32 v18, 1.0, v18
	v_add_f32_e32 v19, 1.0, v19
	v_rcp_f32_e32 v18, v18
	v_rcp_f32_e32 v19, v19
	s_nop 0
	v_pk_mul_f32 v[14:15], v[14:15], v[18:19]
	v_add_f32_e32 v18, 1.0, v23
	v_rcp_f32_e32 v23, v18
	s_nop 0
	v_pk_mul_f32 v[18:19], v[10:11], v[22:23]
	v_add_f32_e32 v11, 1.0, v24
	v_add_f32_e32 v10, 1.0, v20
	v_rcp_f32_e32 v20, v11
	v_add_f32_e32 v11, 1.0, v21
	v_rcp_f32_e32 v10, v10
	v_rcp_f32_e32 v11, v11
	s_nop 0
	v_pk_mul_f32 v[16:17], v[16:17], v[10:11]
	v_add_f32_e32 v10, 1.0, v25
	v_rcp_f32_e32 v21, v10
	v_cvt_pk_bf16_f32 v10, v14, v15
	v_add_co_u32_e32 v14, vcc, s9, v144
	v_pk_mul_f32 v[20:21], v[12:13], v[20:21]
	v_cvt_pk_bf16_f32 v11, v16, v17
	v_cvt_pk_bf16_f32 v12, v18, v19
	v_cvt_pk_bf16_f32 v13, v20, v21
	v_addc_co_u32_e32 v15, vcc, 0, v145, vcc
	global_store_dwordx4 v[14:15], v[10:13], off
	v_cvt_pk_f32_fp8_e32 v[16:17], v69
	v_cvt_pk_f32_fp8_sdwa v[18:19], v69 src0_sel:WORD_1
	v_cvt_pk_f32_fp8_e32 v[10:11], v68
	v_cvt_pk_f32_fp8_sdwa v[12:13], v68 src0_sel:WORD_1
	v_add_f32_e32 v16, 1.0, v16
	v_rcp_f32_e32 v16, v16
	v_add_f32_e32 v10, 1.0, v10
	v_add_f32_e32 v11, 1.0, v11
	v_rcp_f32_e32 v10, v10
	v_rcp_f32_e32 v11, v11
	s_and_b64 vcc, exec, s[6:7]
	v_pk_mul_f32 v[6:7], v[6:7], v[10:11]
	v_add_f32_e32 v10, 1.0, v17
	v_rcp_f32_e32 v17, v10
	s_nop 0
	v_pk_mul_f32 v[10:11], v[2:3], v[16:17]
	v_add_f32_e32 v3, 1.0, v18
	v_add_f32_e32 v2, 1.0, v12
	v_rcp_f32_e32 v12, v3
	v_add_f32_e32 v3, 1.0, v13
	v_rcp_f32_e32 v2, v2
	v_rcp_f32_e32 v3, v3
	s_nop 0
	v_pk_mul_f32 v[8:9], v[8:9], v[2:3]
	v_add_f32_e32 v2, 1.0, v19
	v_rcp_f32_e32 v13, v2
	v_cvt_pk_bf16_f32 v2, v6, v7
	v_cvt_pk_bf16_f32 v3, v8, v9
	v_pk_mul_f32 v[12:13], v[4:5], v[12:13]
	v_cvt_pk_bf16_f32 v4, v10, v11
	v_cvt_pk_bf16_f32 v5, v12, v13
	global_store_dwordx4 v[14:15], v[2:5], off offset:16
	s_cbranch_vccnz .LBB0_872

.LBB0_870:
	s_add_i32 s57, s57, 2
	s_and_b32 s58, s57, 10
	s_cmp_lg_u32 s58, 8
	s_cbranch_scc1 .LBB0_869
	s_cmpk_eq_i32 s64, 0x400
	s_cselect_b32 s58, 0, 0x400
	s_add_u32 s66, s16, s58
	v_mov_b32_e32 v130, v183
	s_addc_u32 s67, s17, 0
	global_load_dwordx4 v[156:159], v130, s[66:67] offset:1536 nt
	global_load_dwordx4 v[160:163], v130, s[66:67] offset:2560 nt
	v_add_u32_e32 v132, 0x1e000, v130
	global_load_dwordx4 v[148:151], v132, s[66:67] offset:1536 nt
	global_load_dwordx4 v[152:155], v132, s[66:67] offset:2560 nt
	v_add_u32_e32 v132, 0x3c000, v130
	global_load_dwordx4 v[144:147], v132, s[66:67] offset:1536 nt
	global_load_dwordx4 v[140:143], v132, s[66:67] offset:2560 nt
	v_add_u32_e32 v136, 0x5a000, v130
	global_load_dwordx4 v[132:135], v136, s[66:67] offset:1536 nt
	s_nop 0
	global_load_dwordx4 v[136:139], v136, s[66:67] offset:2560 nt
	s_waitcnt vmcnt(0)
	v_cvt_pk_f32_fp8_e32 v[186:187], v156
	v_cvt_pk_f32_fp8_sdwa v[188:189], v156 src0_sel:WORD_1
	v_cvt_pk_f32_fp8_e32 v[190:191], v160
	v_cvt_pk_f32_fp8_sdwa v[192:193], v160 src0_sel:WORD_1
	v_add_f32_e32 v156, 1.0, v186
	v_rcp_f32_e32 v186, v156
	v_add_f32_e32 v156, 1.0, v187
	v_rcp_f32_e32 v187, v156
	v_add_f32_e32 v156, 1.0, v188
	v_rcp_f32_e32 v188, v156
	v_add_f32_e32 v156, 1.0, v189
	v_pk_add_f32 v[190:191], v[190:191], 1.0 op_sel_hi:[1,0]
	v_rcp_f32_e32 v189, v156
	v_pk_mul_f32 v[186:187], v[186:187], v[190:191]
	v_pk_add_f32 v[192:193], v[192:193], 1.0 op_sel_hi:[1,0]
	v_pk_mul_f32 v[126:127], v[126:127], v[186:187]
	v_cvt_pk_f32_fp8_e32 v[186:187], v157
	v_cvt_pk_f32_fp8_sdwa v[156:157], v157 src0_sel:WORD_1
	v_pk_mul_f32 v[188:189], v[188:189], v[192:193]
	v_add_f32_e32 v186, 1.0, v186
	v_pk_mul_f32 v[128:129], v[128:129], v[188:189]
	v_cvt_pk_f32_fp8_e32 v[188:189], v161
	v_cvt_pk_f32_fp8_sdwa v[160:161], v161 src0_sel:WORD_1
	v_add_f32_e32 v156, 1.0, v156
	v_add_f32_e32 v157, 1.0, v157
	v_rcp_f32_e32 v156, v156
	v_rcp_f32_e32 v157, v157
	v_add_f32_e32 v187, 1.0, v187
	v_pk_add_f32 v[160:161], v[160:161], 1.0 op_sel_hi:[1,0]
	v_rcp_f32_e32 v186, v186
	v_rcp_f32_e32 v187, v187
	v_pk_mul_f32 v[156:157], v[156:157], v[160:161]
	v_pk_add_f32 v[188:189], v[188:189], 1.0 op_sel_hi:[1,0]
	v_pk_mul_f32 v[124:125], v[124:125], v[156:157]
	v_cvt_pk_f32_fp8_e32 v[156:157], v158
	v_pk_mul_f32 v[186:187], v[186:187], v[188:189]
	v_cvt_pk_f32_fp8_sdwa v[160:161], v158 src0_sel:WORD_1
	v_pk_mul_f32 v[122:123], v[122:123], v[186:187]
	v_cvt_pk_f32_fp8_e32 v[186:187], v162
	v_add_f32_e32 v156, 1.0, v156
	v_add_f32_e32 v157, 1.0, v157
	v_rcp_f32_e32 v156, v156
	v_rcp_f32_e32 v157, v157
	v_add_f32_e32 v158, 1.0, v160
	v_cvt_pk_f32_fp8_sdwa v[188:189], v162 src0_sel:WORD_1
	v_rcp_f32_e32 v160, v158
	v_add_f32_e32 v158, 1.0, v161
	v_pk_add_f32 v[186:187], v[186:187], 1.0 op_sel_hi:[1,0]
	v_rcp_f32_e32 v161, v158
	v_pk_mul_f32 v[156:157], v[156:157], v[186:187]
	v_pk_add_f32 v[188:189], v[188:189], 1.0 op_sel_hi:[1,0]
	v_pk_mul_f32 v[118:119], v[118:119], v[156:157]
	v_cvt_pk_f32_fp8_e32 v[156:157], v159
	v_pk_mul_f32 v[160:161], v[160:161], v[188:189]
	v_cvt_pk_f32_fp8_sdwa v[158:159], v159 src0_sel:WORD_1
	v_pk_mul_f32 v[120:121], v[120:121], v[160:161]
	v_cvt_pk_f32_fp8_e32 v[160:161], v163
	v_add_f32_e32 v156, 1.0, v156
	v_add_f32_e32 v157, 1.0, v157
	v_rcp_f32_e32 v156, v156
	v_rcp_f32_e32 v157, v157
	v_cvt_pk_f32_fp8_sdwa v[162:163], v163 src0_sel:WORD_1
	v_add_f32_e32 v158, 1.0, v158
	v_add_f32_e32 v159, 1.0, v159
	v_pk_add_f32 v[160:161], v[160:161], 1.0 op_sel_hi:[1,0]
	v_rcp_f32_e32 v158, v158
	v_rcp_f32_e32 v159, v159
	v_pk_mul_f32 v[156:157], v[156:157], v[160:161]
	v_pk_add_f32 v[162:163], v[162:163], 1.0 op_sel_hi:[1,0]
	v_pk_mul_f32 v[114:115], v[114:115], v[156:157]
	v_cvt_pk_f32_fp8_e32 v[156:157], v148
	v_pk_mul_f32 v[158:159], v[158:159], v[162:163]
	v_cvt_pk_f32_fp8_e32 v[160:161], v152
	v_pk_mul_f32 v[116:117], v[116:117], v[158:159]
	v_cvt_pk_f32_fp8_sdwa v[158:159], v148 src0_sel:WORD_1
	v_add_f32_e32 v148, 1.0, v156
	v_rcp_f32_e32 v156, v148
	v_add_f32_e32 v148, 1.0, v157
	v_rcp_f32_e32 v157, v148
	v_add_f32_e32 v148, 1.0, v158
	v_cvt_pk_f32_fp8_sdwa v[162:163], v152 src0_sel:WORD_1
	v_rcp_f32_e32 v158, v148
	v_add_f32_e32 v148, 1.0, v159
	v_pk_add_f32 v[160:161], v[160:161], 1.0 op_sel_hi:[1,0]
	v_rcp_f32_e32 v159, v148
	v_pk_mul_f32 v[156:157], v[156:157], v[160:161]
	v_pk_add_f32 v[162:163], v[162:163], 1.0 op_sel_hi:[1,0]
	v_pk_mul_f32 v[110:111], v[110:111], v[156:157]
	v_cvt_pk_f32_fp8_e32 v[156:157], v149
	v_cvt_pk_f32_fp8_sdwa v[148:149], v149 src0_sel:WORD_1
	v_pk_mul_f32 v[158:159], v[158:159], v[162:163]
	v_add_f32_e32 v156, 1.0, v156
	v_pk_mul_f32 v[112:113], v[112:113], v[158:159]
	v_cvt_pk_f32_fp8_e32 v[158:159], v153
	v_cvt_pk_f32_fp8_sdwa v[152:153], v153 src0_sel:WORD_1
	v_add_f32_e32 v148, 1.0, v148
	v_add_f32_e32 v149, 1.0, v149
	v_rcp_f32_e32 v148, v148
	v_rcp_f32_e32 v149, v149
	v_add_f32_e32 v157, 1.0, v157
	v_pk_add_f32 v[152:153], v[152:153], 1.0 op_sel_hi:[1,0]
	v_rcp_f32_e32 v156, v156
	v_rcp_f32_e32 v157, v157
	v_pk_mul_f32 v[148:149], v[148:149], v[152:153]
	v_pk_add_f32 v[158:159], v[158:159], 1.0 op_sel_hi:[1,0]
	v_pk_mul_f32 v[108:109], v[108:109], v[148:149]
	v_cvt_pk_f32_fp8_e32 v[148:149], v150
	v_pk_mul_f32 v[156:157], v[156:157], v[158:159]
	v_cvt_pk_f32_fp8_sdwa v[152:153], v150 src0_sel:WORD_1
	v_pk_mul_f32 v[106:107], v[106:107], v[156:157]
	v_cvt_pk_f32_fp8_e32 v[156:157], v154
	v_add_f32_e32 v148, 1.0, v148
	v_add_f32_e32 v149, 1.0, v149
	v_rcp_f32_e32 v148, v148
	v_rcp_f32_e32 v149, v149
	v_add_f32_e32 v150, 1.0, v152
	v_cvt_pk_f32_fp8_sdwa v[158:159], v154 src0_sel:WORD_1
	v_rcp_f32_e32 v152, v150
	v_add_f32_e32 v150, 1.0, v153
	v_pk_add_f32 v[156:157], v[156:157], 1.0 op_sel_hi:[1,0]
	v_rcp_f32_e32 v153, v150
	v_pk_mul_f32 v[148:149], v[148:149], v[156:157]
	v_pk_add_f32 v[158:159], v[158:159], 1.0 op_sel_hi:[1,0]
	v_pk_mul_f32 v[102:103], v[102:103], v[148:149]
	v_cvt_pk_f32_fp8_e32 v[148:149], v151
	v_pk_mul_f32 v[152:153], v[152:153], v[158:159]
	v_cvt_pk_f32_fp8_sdwa v[150:151], v151 src0_sel:WORD_1
	v_pk_mul_f32 v[104:105], v[104:105], v[152:153]
	v_cvt_pk_f32_fp8_e32 v[152:153], v155
	v_add_f32_e32 v148, 1.0, v148
	v_add_f32_e32 v149, 1.0, v149
	v_rcp_f32_e32 v148, v148
	v_rcp_f32_e32 v149, v149
	v_cvt_pk_f32_fp8_sdwa v[154:155], v155 src0_sel:WORD_1
	v_add_f32_e32 v150, 1.0, v150
	v_add_f32_e32 v151, 1.0, v151
	v_pk_add_f32 v[152:153], v[152:153], 1.0 op_sel_hi:[1,0]
	v_rcp_f32_e32 v150, v150
	v_rcp_f32_e32 v151, v151
	v_pk_mul_f32 v[148:149], v[148:149], v[152:153]
	v_pk_add_f32 v[154:155], v[154:155], 1.0 op_sel_hi:[1,0]
	v_pk_mul_f32 v[98:99], v[98:99], v[148:149]
	v_cvt_pk_f32_fp8_e32 v[148:149], v144
	v_pk_mul_f32 v[150:151], v[150:151], v[154:155]
	v_cvt_pk_f32_fp8_e32 v[152:153], v140
	v_pk_mul_f32 v[100:101], v[100:101], v[150:151]
	v_cvt_pk_f32_fp8_sdwa v[150:151], v144 src0_sel:WORD_1
	v_cvt_pk_f32_fp8_sdwa v[154:155], v140 src0_sel:WORD_1
	v_add_f32_e32 v140, 1.0, v148
	v_rcp_f32_e32 v148, v140
	v_add_f32_e32 v140, 1.0, v149
	v_rcp_f32_e32 v149, v140
	v_add_f32_e32 v140, 1.0, v150
	v_rcp_f32_e32 v150, v140
	v_add_f32_e32 v140, 1.0, v151
	v_pk_add_f32 v[152:153], v[152:153], 1.0 op_sel_hi:[1,0]
	v_rcp_f32_e32 v151, v140
	v_pk_mul_f32 v[148:149], v[148:149], v[152:153]
	v_pk_add_f32 v[154:155], v[154:155], 1.0 op_sel_hi:[1,0]
	v_pk_mul_f32 v[94:95], v[94:95], v[148:149]
	v_cvt_pk_f32_fp8_e32 v[148:149], v145
	v_cvt_pk_f32_fp8_sdwa v[144:145], v145 src0_sel:WORD_1
	v_pk_mul_f32 v[150:151], v[150:151], v[154:155]
	v_add_f32_e32 v148, 1.0, v148
	v_pk_mul_f32 v[96:97], v[96:97], v[150:151]
	v_cvt_pk_f32_fp8_e32 v[150:151], v141
	v_cvt_pk_f32_fp8_sdwa v[140:141], v141 src0_sel:WORD_1
	v_add_f32_e32 v144, 1.0, v144
	v_add_f32_e32 v145, 1.0, v145
	v_rcp_f32_e32 v144, v144
	v_rcp_f32_e32 v145, v145
	v_add_f32_e32 v149, 1.0, v149
	v_pk_add_f32 v[140:141], v[140:141], 1.0 op_sel_hi:[1,0]
	v_rcp_f32_e32 v148, v148
	v_rcp_f32_e32 v149, v149
	v_pk_mul_f32 v[140:141], v[144:145], v[140:141]
	v_pk_add_f32 v[150:151], v[150:151], 1.0 op_sel_hi:[1,0]
	v_pk_mul_f32 v[92:93], v[92:93], v[140:141]
	v_cvt_pk_f32_fp8_e32 v[140:141], v146
	v_pk_mul_f32 v[148:149], v[148:149], v[150:151]
	v_cvt_pk_f32_fp8_sdwa v[144:145], v146 src0_sel:WORD_1
	v_pk_mul_f32 v[90:91], v[90:91], v[148:149]
	v_cvt_pk_f32_fp8_e32 v[148:149], v142
	v_add_f32_e32 v140, 1.0, v140
	v_add_f32_e32 v141, 1.0, v141
	v_rcp_f32_e32 v140, v140
	v_rcp_f32_e32 v141, v141
	v_cvt_pk_f32_fp8_sdwa v[150:151], v142 src0_sel:WORD_1
	v_add_f32_e32 v142, 1.0, v144
	v_rcp_f32_e32 v144, v142
	v_add_f32_e32 v142, 1.0, v145
	v_pk_add_f32 v[148:149], v[148:149], 1.0 op_sel_hi:[1,0]
	v_rcp_f32_e32 v145, v142
	v_pk_mul_f32 v[140:141], v[140:141], v[148:149]
	v_pk_add_f32 v[150:151], v[150:151], 1.0 op_sel_hi:[1,0]
	v_pk_mul_f32 v[86:87], v[86:87], v[140:141]
	v_cvt_pk_f32_fp8_e32 v[140:141], v147
	v_pk_mul_f32 v[144:145], v[144:145], v[150:151]
	v_add_f32_e32 v140, 1.0, v140
	v_pk_mul_f32 v[88:89], v[88:89], v[144:145]
	v_cvt_pk_f32_fp8_sdwa v[144:145], v147 src0_sel:WORD_1
	v_cvt_pk_f32_fp8_e32 v[146:147], v143
	v_add_f32_e32 v141, 1.0, v141
	v_rcp_f32_e32 v140, v140
	v_rcp_f32_e32 v141, v141
	v_cvt_pk_f32_fp8_sdwa v[142:143], v143 src0_sel:WORD_1
	v_add_f32_e32 v144, 1.0, v144
	v_add_f32_e32 v145, 1.0, v145
	v_pk_add_f32 v[146:147], v[146:147], 1.0 op_sel_hi:[1,0]
	v_rcp_f32_e32 v144, v144
	v_rcp_f32_e32 v145, v145
	v_pk_mul_f32 v[140:141], v[140:141], v[146:147]
	v_pk_add_f32 v[142:143], v[142:143], 1.0 op_sel_hi:[1,0]
	v_pk_mul_f32 v[82:83], v[82:83], v[140:141]
	v_cvt_pk_f32_fp8_e32 v[140:141], v132
	v_pk_mul_f32 v[142:143], v[144:145], v[142:143]
	v_cvt_pk_f32_fp8_e32 v[144:145], v136
	v_pk_mul_f32 v[84:85], v[84:85], v[142:143]
	v_cvt_pk_f32_fp8_sdwa v[142:143], v132 src0_sel:WORD_1
	v_add_f32_e32 v132, 1.0, v140
	v_rcp_f32_e32 v140, v132
	v_add_f32_e32 v132, 1.0, v141
	v_rcp_f32_e32 v141, v132
	v_add_f32_e32 v132, 1.0, v142
	v_cvt_pk_f32_fp8_sdwa v[146:147], v136 src0_sel:WORD_1
	v_rcp_f32_e32 v142, v132
	v_add_f32_e32 v132, 1.0, v143
	v_pk_add_f32 v[144:145], v[144:145], 1.0 op_sel_hi:[1,0]
	v_rcp_f32_e32 v143, v132
	v_pk_mul_f32 v[140:141], v[140:141], v[144:145]
	v_pk_add_f32 v[146:147], v[146:147], 1.0 op_sel_hi:[1,0]
	v_pk_mul_f32 v[78:79], v[78:79], v[140:141]
	v_cvt_pk_f32_fp8_e32 v[140:141], v133
	v_cvt_pk_f32_fp8_sdwa v[132:133], v133 src0_sel:WORD_1
	v_pk_mul_f32 v[142:143], v[142:143], v[146:147]
	v_add_f32_e32 v140, 1.0, v140
	v_pk_mul_f32 v[80:81], v[80:81], v[142:143]
	v_cvt_pk_f32_fp8_e32 v[142:143], v137
	v_cvt_pk_f32_fp8_sdwa v[136:137], v137 src0_sel:WORD_1
	v_add_f32_e32 v132, 1.0, v132
	v_add_f32_e32 v133, 1.0, v133
	v_rcp_f32_e32 v132, v132
	v_rcp_f32_e32 v133, v133
	v_add_f32_e32 v141, 1.0, v141
	v_pk_add_f32 v[136:137], v[136:137], 1.0 op_sel_hi:[1,0]
	v_rcp_f32_e32 v140, v140
	v_rcp_f32_e32 v141, v141
	v_pk_mul_f32 v[132:133], v[132:133], v[136:137]
	v_pk_add_f32 v[142:143], v[142:143], 1.0 op_sel_hi:[1,0]
	v_pk_mul_f32 v[76:77], v[76:77], v[132:133]
	v_cvt_pk_f32_fp8_e32 v[132:133], v134
	v_pk_mul_f32 v[140:141], v[140:141], v[142:143]
	v_cvt_pk_f32_fp8_sdwa v[136:137], v134 src0_sel:WORD_1
	v_pk_mul_f32 v[74:75], v[74:75], v[140:141]
	v_cvt_pk_f32_fp8_e32 v[140:141], v138
	v_add_f32_e32 v132, 1.0, v132
	v_add_f32_e32 v133, 1.0, v133
	v_rcp_f32_e32 v132, v132
	v_rcp_f32_e32 v133, v133
	v_add_f32_e32 v134, 1.0, v136
	v_cvt_pk_f32_fp8_sdwa v[142:143], v138 src0_sel:WORD_1
	v_rcp_f32_e32 v136, v134
	v_add_f32_e32 v134, 1.0, v137
	v_pk_add_f32 v[140:141], v[140:141], 1.0 op_sel_hi:[1,0]
	v_rcp_f32_e32 v137, v134
	v_pk_mul_f32 v[132:133], v[132:133], v[140:141]
	v_pk_add_f32 v[142:143], v[142:143], 1.0 op_sel_hi:[1,0]
	v_pk_mul_f32 v[70:71], v[70:71], v[132:133]
	v_cvt_pk_f32_fp8_e32 v[132:133], v135
	v_pk_mul_f32 v[136:137], v[136:137], v[142:143]
	v_cvt_pk_f32_fp8_sdwa v[134:135], v135 src0_sel:WORD_1
	v_pk_mul_f32 v[72:73], v[72:73], v[136:137]
	v_cvt_pk_f32_fp8_e32 v[136:137], v139
	v_add_f32_e32 v132, 1.0, v132
	v_add_f32_e32 v133, 1.0, v133
	v_rcp_f32_e32 v132, v132
	v_rcp_f32_e32 v133, v133
	v_pk_add_f32 v[136:137], v[136:137], 1.0 op_sel_hi:[1,0]
	v_cvt_pk_f32_fp8_sdwa v[138:139], v139 src0_sel:WORD_1
	v_add_f32_e32 v134, 1.0, v134
	v_pk_mul_f32 v[132:133], v[132:133], v[136:137]
	v_add_f32_e32 v135, 1.0, v135
	v_pk_mul_f32 v[66:67], v[66:67], v[132:133]
	v_add_u32_e32 v132, 0xf0000, v130
	global_load_dwordx4 v[140:143], v132, s[66:67] offset:1536 nt
	global_load_dwordx4 v[144:147], v132, s[66:67] offset:2560 nt
	v_add_u32_e32 v132, 0x10e000, v130
	global_load_dwordx4 v[156:159], v132, s[66:67] offset:1536 nt
	global_load_dwordx4 v[160:163], v132, s[66:67] offset:2560 nt
	v_rcp_f32_e32 v134, v134
	v_rcp_f32_e32 v135, v135
	v_pk_add_f32 v[138:139], v[138:139], 1.0 op_sel_hi:[1,0]
	v_add_u32_e32 v132, 0x12c000, v130
	v_add_u32_e32 v130, 0x14a000, v130
	v_pk_mul_f32 v[134:135], v[134:135], v[138:139]
	global_load_dwordx4 v[148:151], v132, s[66:67] offset:1536 nt
	global_load_dwordx4 v[152:155], v132, s[66:67] offset:2560 nt
	v_pk_mul_f32 v[68:69], v[68:69], v[134:135]
	global_load_dwordx4 v[132:135], v130, s[66:67] offset:1536 nt
	global_load_dwordx4 v[136:139], v130, s[66:67] offset:2560 nt
	s_waitcnt vmcnt(0)
	v_cvt_pk_f32_fp8_e32 v[186:187], v140
	v_cvt_pk_f32_fp8_e32 v[190:191], v144
	v_cvt_pk_f32_fp8_sdwa v[188:189], v140 src0_sel:WORD_1
	v_cvt_pk_f32_fp8_sdwa v[192:193], v144 src0_sel:WORD_1
	v_add_f32_e32 v130, 1.0, v186
	v_rcp_f32_e32 v186, v130
	v_add_f32_e32 v130, 1.0, v187
	v_rcp_f32_e32 v187, v130
	v_pk_add_f32 v[190:191], v[190:191], 1.0 op_sel_hi:[1,0]
	v_add_f32_e32 v130, 1.0, v188
	v_rcp_f32_e32 v188, v130
	v_pk_mul_f32 v[186:187], v[186:187], v[190:191]
	v_add_f32_e32 v130, 1.0, v189
	v_pk_mul_f32 v[62:63], v[62:63], v[186:187]
	v_cvt_pk_f32_fp8_e32 v[186:187], v141
	v_rcp_f32_e32 v189, v130
	v_cvt_pk_f32_fp8_sdwa v[140:141], v141 src0_sel:WORD_1
	v_pk_add_f32 v[192:193], v[192:193], 1.0 op_sel_hi:[1,0]
	v_add_f32_e32 v130, 1.0, v186
	v_rcp_f32_e32 v186, v130
	v_add_f32_e32 v130, 1.0, v187
	v_pk_mul_f32 v[188:189], v[188:189], v[192:193]
	v_rcp_f32_e32 v187, v130
	v_add_f32_e32 v130, 1.0, v140
	v_pk_mul_f32 v[64:65], v[64:65], v[188:189]
	v_cvt_pk_f32_fp8_e32 v[188:189], v145
	v_cvt_pk_f32_fp8_sdwa v[144:145], v145 src0_sel:WORD_1
	v_rcp_f32_e32 v140, v130
	v_add_f32_e32 v130, 1.0, v141
	v_rcp_f32_e32 v141, v130
	v_pk_add_f32 v[144:145], v[144:145], 1.0 op_sel_hi:[1,0]
	v_pk_add_f32 v[188:189], v[188:189], 1.0 op_sel_hi:[1,0]
	v_pk_mul_f32 v[140:141], v[140:141], v[144:145]
	s_nop 0
	v_pk_mul_f32 v[60:61], v[60:61], v[140:141]
	v_cvt_pk_f32_fp8_e32 v[140:141], v142
	v_pk_mul_f32 v[186:187], v[186:187], v[188:189]
	v_cvt_pk_f32_fp8_sdwa v[144:145], v142 src0_sel:WORD_1
	v_pk_mul_f32 v[58:59], v[58:59], v[186:187]
	v_add_f32_e32 v130, 1.0, v140
	v_cvt_pk_f32_fp8_e32 v[186:187], v146
	v_rcp_f32_e32 v140, v130
	v_add_f32_e32 v130, 1.0, v141
	v_rcp_f32_e32 v141, v130
	v_add_f32_e32 v130, 1.0, v144
	v_pk_add_f32 v[186:187], v[186:187], 1.0 op_sel_hi:[1,0]
	v_cvt_pk_f32_fp8_sdwa v[188:189], v146 src0_sel:WORD_1
	v_rcp_f32_e32 v144, v130
	v_add_f32_e32 v130, 1.0, v145
	v_pk_mul_f32 v[140:141], v[140:141], v[186:187]
	v_rcp_f32_e32 v145, v130
	v_pk_mul_f32 v[54:55], v[54:55], v[140:141]
	v_cvt_pk_f32_fp8_e32 v[140:141], v143
	v_pk_add_f32 v[188:189], v[188:189], 1.0 op_sel_hi:[1,0]
	v_cvt_pk_f32_fp8_sdwa v[142:143], v143 src0_sel:WORD_1
	v_pk_mul_f32 v[144:145], v[144:145], v[188:189]
	v_add_f32_e32 v130, 1.0, v140
	v_pk_mul_f32 v[56:57], v[56:57], v[144:145]
	v_cvt_pk_f32_fp8_e32 v[144:145], v147
	v_rcp_f32_e32 v140, v130
	v_add_f32_e32 v130, 1.0, v141
	v_rcp_f32_e32 v141, v130
	v_pk_add_f32 v[144:145], v[144:145], 1.0 op_sel_hi:[1,0]
	v_add_f32_e32 v130, 1.0, v142
	v_cvt_pk_f32_fp8_sdwa v[146:147], v147 src0_sel:WORD_1
	v_pk_mul_f32 v[140:141], v[140:141], v[144:145]
	v_rcp_f32_e32 v142, v130
	v_pk_mul_f32 v[50:51], v[50:51], v[140:141]
	v_cvt_pk_f32_fp8_e32 v[140:141], v156
	v_add_f32_e32 v130, 1.0, v143
	v_rcp_f32_e32 v143, v130
	v_pk_add_f32 v[146:147], v[146:147], 1.0 op_sel_hi:[1,0]
	v_add_f32_e32 v130, 1.0, v140
	v_cvt_pk_f32_fp8_e32 v[144:145], v160
	v_rcp_f32_e32 v140, v130
	v_add_f32_e32 v130, 1.0, v141
	v_pk_mul_f32 v[142:143], v[142:143], v[146:147]
	v_rcp_f32_e32 v141, v130
	v_pk_mul_f32 v[52:53], v[52:53], v[142:143]
	v_cvt_pk_f32_fp8_sdwa v[142:143], v156 src0_sel:WORD_1
	v_pk_add_f32 v[144:145], v[144:145], 1.0 op_sel_hi:[1,0]
	v_cvt_pk_f32_fp8_sdwa v[146:147], v160 src0_sel:WORD_1
	v_pk_mul_f32 v[140:141], v[140:141], v[144:145]
	v_add_f32_e32 v130, 1.0, v142
	v_pk_mul_f32 v[46:47], v[46:47], v[140:141]
	v_cvt_pk_f32_fp8_e32 v[140:141], v157
	v_rcp_f32_e32 v142, v130
	v_add_f32_e32 v130, 1.0, v143
	v_rcp_f32_e32 v143, v130
	v_add_f32_e32 v130, 1.0, v140
	v_pk_add_f32 v[146:147], v[146:147], 1.0 op_sel_hi:[1,0]
	v_cvt_pk_f32_fp8_e32 v[144:145], v161
	v_rcp_f32_e32 v140, v130
	v_add_f32_e32 v130, 1.0, v141
	v_pk_mul_f32 v[142:143], v[142:143], v[146:147]
	v_rcp_f32_e32 v141, v130
	v_pk_mul_f32 v[48:49], v[48:49], v[142:143]
	v_cvt_pk_f32_fp8_sdwa v[142:143], v157 src0_sel:WORD_1
	v_pk_add_f32 v[144:145], v[144:145], 1.0 op_sel_hi:[1,0]
	v_cvt_pk_f32_fp8_sdwa v[146:147], v161 src0_sel:WORD_1
	v_pk_mul_f32 v[140:141], v[140:141], v[144:145]
	v_add_f32_e32 v130, 1.0, v142
	v_pk_mul_f32 v[42:43], v[42:43], v[140:141]
	v_cvt_pk_f32_fp8_e32 v[140:141], v158
	v_rcp_f32_e32 v142, v130
	v_add_f32_e32 v130, 1.0, v143
	v_rcp_f32_e32 v143, v130
	v_add_f32_e32 v130, 1.0, v140
	v_pk_add_f32 v[146:147], v[146:147], 1.0 op_sel_hi:[1,0]
	v_cvt_pk_f32_fp8_e32 v[144:145], v162
	v_rcp_f32_e32 v140, v130
	v_add_f32_e32 v130, 1.0, v141
	v_pk_mul_f32 v[142:143], v[142:143], v[146:147]
	v_rcp_f32_e32 v141, v130
	v_pk_mul_f32 v[44:45], v[44:45], v[142:143]
	v_cvt_pk_f32_fp8_sdwa v[142:143], v158 src0_sel:WORD_1
	v_pk_add_f32 v[144:145], v[144:145], 1.0 op_sel_hi:[1,0]
	v_cvt_pk_f32_fp8_sdwa v[146:147], v162 src0_sel:WORD_1
	v_pk_mul_f32 v[140:141], v[140:141], v[144:145]
	v_add_f32_e32 v130, 1.0, v142
	v_pk_mul_f32 v[38:39], v[38:39], v[140:141]
	v_cvt_pk_f32_fp8_e32 v[140:141], v159
	v_rcp_f32_e32 v142, v130
	v_add_f32_e32 v130, 1.0, v143
	v_rcp_f32_e32 v143, v130
	v_add_f32_e32 v130, 1.0, v140
	v_pk_add_f32 v[146:147], v[146:147], 1.0 op_sel_hi:[1,0]
	v_cvt_pk_f32_fp8_e32 v[144:145], v163
	v_rcp_f32_e32 v140, v130
	v_add_f32_e32 v130, 1.0, v141
	v_pk_mul_f32 v[142:143], v[142:143], v[146:147]
	v_rcp_f32_e32 v141, v130
	v_pk_mul_f32 v[40:41], v[40:41], v[142:143]
	v_cvt_pk_f32_fp8_sdwa v[142:143], v159 src0_sel:WORD_1
	v_pk_add_f32 v[144:145], v[144:145], 1.0 op_sel_hi:[1,0]
	v_cvt_pk_f32_fp8_sdwa v[146:147], v163 src0_sel:WORD_1
	v_pk_mul_f32 v[140:141], v[140:141], v[144:145]
	v_add_f32_e32 v130, 1.0, v142
	v_pk_mul_f32 v[34:35], v[34:35], v[140:141]
	v_cvt_pk_f32_fp8_e32 v[140:141], v148
	v_rcp_f32_e32 v142, v130
	v_add_f32_e32 v130, 1.0, v143
	v_rcp_f32_e32 v143, v130
	v_add_f32_e32 v130, 1.0, v140
	v_pk_add_f32 v[146:147], v[146:147], 1.0 op_sel_hi:[1,0]
	v_cvt_pk_f32_fp8_e32 v[144:145], v152
	v_rcp_f32_e32 v140, v130
	v_add_f32_e32 v130, 1.0, v141
	v_pk_mul_f32 v[142:143], v[142:143], v[146:147]
	v_rcp_f32_e32 v141, v130
	v_pk_mul_f32 v[36:37], v[36:37], v[142:143]
	v_cvt_pk_f32_fp8_sdwa v[142:143], v148 src0_sel:WORD_1
	v_pk_add_f32 v[144:145], v[144:145], 1.0 op_sel_hi:[1,0]
	v_cvt_pk_f32_fp8_sdwa v[146:147], v152 src0_sel:WORD_1
	v_pk_mul_f32 v[140:141], v[140:141], v[144:145]
	v_add_f32_e32 v130, 1.0, v142
	v_pk_mul_f32 v[30:31], v[30:31], v[140:141]
	v_cvt_pk_f32_fp8_e32 v[140:141], v149
	v_rcp_f32_e32 v142, v130
	v_add_f32_e32 v130, 1.0, v143
	v_rcp_f32_e32 v143, v130
	v_add_f32_e32 v130, 1.0, v140
	v_pk_add_f32 v[146:147], v[146:147], 1.0 op_sel_hi:[1,0]
	v_cvt_pk_f32_fp8_e32 v[144:145], v153
	v_rcp_f32_e32 v140, v130
	v_add_f32_e32 v130, 1.0, v141
	v_pk_mul_f32 v[142:143], v[142:143], v[146:147]
	v_rcp_f32_e32 v141, v130
	v_pk_mul_f32 v[32:33], v[32:33], v[142:143]
	v_cvt_pk_f32_fp8_sdwa v[142:143], v149 src0_sel:WORD_1
	v_pk_add_f32 v[144:145], v[144:145], 1.0 op_sel_hi:[1,0]
	v_cvt_pk_f32_fp8_sdwa v[146:147], v153 src0_sel:WORD_1
	v_pk_mul_f32 v[140:141], v[140:141], v[144:145]
	v_add_f32_e32 v130, 1.0, v142
	v_pk_mul_f32 v[26:27], v[26:27], v[140:141]
	v_cvt_pk_f32_fp8_e32 v[140:141], v150
	v_rcp_f32_e32 v142, v130
	v_add_f32_e32 v130, 1.0, v143
	v_rcp_f32_e32 v143, v130
	v_add_f32_e32 v130, 1.0, v140
	v_pk_add_f32 v[146:147], v[146:147], 1.0 op_sel_hi:[1,0]
	v_cvt_pk_f32_fp8_e32 v[144:145], v154
	v_rcp_f32_e32 v140, v130
	v_add_f32_e32 v130, 1.0, v141
	v_pk_mul_f32 v[142:143], v[142:143], v[146:147]
	v_rcp_f32_e32 v141, v130
	v_pk_mul_f32 v[28:29], v[28:29], v[142:143]
	v_cvt_pk_f32_fp8_sdwa v[142:143], v150 src0_sel:WORD_1
	v_pk_add_f32 v[144:145], v[144:145], 1.0 op_sel_hi:[1,0]
	v_cvt_pk_f32_fp8_sdwa v[146:147], v154 src0_sel:WORD_1
	v_pk_mul_f32 v[140:141], v[140:141], v[144:145]
	v_add_f32_e32 v130, 1.0, v142
	v_pk_mul_f32 v[22:23], v[22:23], v[140:141]
	v_cvt_pk_f32_fp8_e32 v[140:141], v151
	v_rcp_f32_e32 v142, v130
	v_add_f32_e32 v130, 1.0, v143
	v_rcp_f32_e32 v143, v130
	v_add_f32_e32 v130, 1.0, v140
	v_pk_add_f32 v[146:147], v[146:147], 1.0 op_sel_hi:[1,0]
	v_cvt_pk_f32_fp8_e32 v[144:145], v155
	v_rcp_f32_e32 v140, v130
	v_add_f32_e32 v130, 1.0, v141
	v_pk_mul_f32 v[142:143], v[142:143], v[146:147]
	v_rcp_f32_e32 v141, v130
	v_pk_mul_f32 v[24:25], v[24:25], v[142:143]
	v_cvt_pk_f32_fp8_sdwa v[142:143], v151 src0_sel:WORD_1
	v_pk_add_f32 v[144:145], v[144:145], 1.0 op_sel_hi:[1,0]
	v_cvt_pk_f32_fp8_sdwa v[146:147], v155 src0_sel:WORD_1
	v_pk_mul_f32 v[140:141], v[140:141], v[144:145]
	v_add_f32_e32 v130, 1.0, v142
	v_pk_mul_f32 v[18:19], v[18:19], v[140:141]
	v_cvt_pk_f32_fp8_e32 v[140:141], v132
	v_rcp_f32_e32 v142, v130
	v_add_f32_e32 v130, 1.0, v143
	v_rcp_f32_e32 v143, v130
	v_add_f32_e32 v130, 1.0, v140
	v_pk_add_f32 v[146:147], v[146:147], 1.0 op_sel_hi:[1,0]
	v_cvt_pk_f32_fp8_e32 v[144:145], v136
	v_rcp_f32_e32 v140, v130
	v_add_f32_e32 v130, 1.0, v141
	v_pk_mul_f32 v[142:143], v[142:143], v[146:147]
	v_rcp_f32_e32 v141, v130
	v_pk_mul_f32 v[20:21], v[20:21], v[142:143]
	v_cvt_pk_f32_fp8_sdwa v[142:143], v132 src0_sel:WORD_1
	v_pk_add_f32 v[144:145], v[144:145], 1.0 op_sel_hi:[1,0]
	v_cvt_pk_f32_fp8_sdwa v[146:147], v136 src0_sel:WORD_1
	v_pk_mul_f32 v[140:141], v[140:141], v[144:145]
	v_add_f32_e32 v130, 1.0, v142
	v_pk_mul_f32 v[14:15], v[14:15], v[140:141]
	v_cvt_pk_f32_fp8_e32 v[140:141], v133
	v_rcp_f32_e32 v142, v130
	v_add_f32_e32 v130, 1.0, v143
	v_rcp_f32_e32 v143, v130
	v_cvt_pk_f32_fp8_sdwa v[132:133], v133 src0_sel:WORD_1
	v_add_f32_e32 v130, 1.0, v140
	v_pk_add_f32 v[146:147], v[146:147], 1.0 op_sel_hi:[1,0]
	v_rcp_f32_e32 v140, v130
	v_add_f32_e32 v130, 1.0, v141
	v_pk_mul_f32 v[142:143], v[142:143], v[146:147]
	v_rcp_f32_e32 v141, v130
	v_add_f32_e32 v130, 1.0, v132
	v_pk_mul_f32 v[16:17], v[16:17], v[142:143]
	v_cvt_pk_f32_fp8_e32 v[142:143], v137
	v_cvt_pk_f32_fp8_sdwa v[136:137], v137 src0_sel:WORD_1
	v_rcp_f32_e32 v132, v130
	v_add_f32_e32 v130, 1.0, v133
	v_rcp_f32_e32 v133, v130
	v_pk_add_f32 v[136:137], v[136:137], 1.0 op_sel_hi:[1,0]
	v_pk_add_f32 v[142:143], v[142:143], 1.0 op_sel_hi:[1,0]
	v_pk_mul_f32 v[132:133], v[132:133], v[136:137]
	s_nop 0
	v_pk_mul_f32 v[12:13], v[12:13], v[132:133]
	v_cvt_pk_f32_fp8_e32 v[132:133], v134
	v_pk_mul_f32 v[140:141], v[140:141], v[142:143]
	v_cvt_pk_f32_fp8_sdwa v[136:137], v134 src0_sel:WORD_1
	v_pk_mul_f32 v[10:11], v[10:11], v[140:141]
	v_add_f32_e32 v130, 1.0, v132
	v_cvt_pk_f32_fp8_e32 v[140:141], v138
	v_rcp_f32_e32 v132, v130
	v_add_f32_e32 v130, 1.0, v133
	v_rcp_f32_e32 v133, v130
	v_pk_add_f32 v[140:141], v[140:141], 1.0 op_sel_hi:[1,0]
	v_add_f32_e32 v130, 1.0, v136
	v_cvt_pk_f32_fp8_sdwa v[142:143], v138 src0_sel:WORD_1
	v_pk_mul_f32 v[132:133], v[132:133], v[140:141]
	v_rcp_f32_e32 v136, v130
	v_pk_mul_f32 v[6:7], v[6:7], v[132:133]
	v_cvt_pk_f32_fp8_e32 v[132:133], v135
	v_add_f32_e32 v130, 1.0, v137
	v_rcp_f32_e32 v137, v130
	v_cvt_pk_f32_fp8_sdwa v[134:135], v135 src0_sel:WORD_1
	v_add_f32_e32 v130, 1.0, v132
	v_pk_add_f32 v[142:143], v[142:143], 1.0 op_sel_hi:[1,0]
	v_rcp_f32_e32 v132, v130
	v_add_f32_e32 v130, 1.0, v133
	v_pk_mul_f32 v[136:137], v[136:137], v[142:143]
	v_rcp_f32_e32 v133, v130
	v_add_f32_e32 v130, 1.0, v134
	v_pk_mul_f32 v[8:9], v[8:9], v[136:137]
	v_cvt_pk_f32_fp8_e32 v[136:137], v139
	v_cvt_pk_f32_fp8_sdwa v[138:139], v139 src0_sel:WORD_1
	v_rcp_f32_e32 v134, v130
	v_add_f32_e32 v130, 1.0, v135
	v_rcp_f32_e32 v135, v130
	v_pk_add_f32 v[138:139], v[138:139], 1.0 op_sel_hi:[1,0]
	v_pk_add_f32 v[136:137], v[136:137], 1.0 op_sel_hi:[1,0]
	v_pk_mul_f32 v[134:135], v[134:135], v[138:139]
	v_pk_mul_f32 v[132:133], v[132:133], v[136:137]
	v_pk_mul_f32 v[4:5], v[4:5], v[134:135]
	v_pk_mul_f32 v[2:3], v[2:3], v[132:133]
	s_branch .LBB0_869

.LBB0_1095:
	v_mov_b32_e32 v132, v184
	v_mov_b32_e32 v130, v183
	global_load_dwordx4 v[148:151], v130, s[14:15] offset:3584 nt
	s_lshl_b64 s[12:13], s[16:17], 11
	s_add_u32 s7, s44, s12
	s_addc_u32 s16, s45, s13
	s_lshl_b64 s[12:13], s[18:19], 1
	s_add_u32 s12, s7, s12
	s_addc_u32 s13, s16, s13
	v_lshl_add_u64 v[146:147], s[14:15], 0, v[130:131]
	v_mov_b32_e32 v133, v131
	s_mov_b32 s7, 0x1e000
	v_lshl_add_u64 v[144:145], v[132:133], 1, s[12:13]
	v_add_co_u32_e32 v132, vcc, s7, v146
	s_mov_b32 s7, 0x3c000
	s_nop 0
	v_addc_co_u32_e32 v133, vcc, 0, v147, vcc
	global_load_dwordx4 v[140:143], v[132:133], off offset:3584 nt
	v_add_co_u32_e32 v132, vcc, s7, v146
	s_mov_b32 s7, 0x5a000
	s_nop 0
	v_addc_co_u32_e32 v133, vcc, 0, v147, vcc
	global_load_dwordx4 v[136:139], v[132:133], off offset:3584 nt
	v_add_co_u32_e32 v132, vcc, s7, v146
	s_mov_b32 s7, 0x8000
	s_nop 0
	v_addc_co_u32_e32 v133, vcc, 0, v147, vcc
	global_load_dwordx4 v[132:135], v[132:133], off offset:3584 nt
	s_mov_b32 s14, s6
	s_mov_b32 s15, s51
	s_mov_b64 s[62:63], s[10:11]
	s_mov_b64 s[12:13], s[8:9]
	s_mov_b32 s53, 0x42b17218
	s_waitcnt vmcnt(0)
	v_cvt_pk_f32_fp8_e32 v[152:153], v148
	v_cvt_pk_f32_fp8_e32 v[156:157], v149
	v_cvt_pk_f32_fp8_sdwa v[154:155], v148 src0_sel:WORD_1
	v_cvt_pk_f32_fp8_sdwa v[148:149], v149 src0_sel:WORD_1
	v_add_f32_e32 v130, 1.0, v152
	v_rcp_f32_e32 v152, v130
	v_add_f32_e32 v130, 1.0, v156
	v_rcp_f32_e32 v156, v130
	v_add_f32_e32 v130, 1.0, v153
	v_rcp_f32_e32 v153, v130
	v_add_f32_e32 v130, 1.0, v157
	v_rcp_f32_e32 v157, v130
	v_pk_mul_f32 v[126:127], v[126:127], v[152:153]
	v_pk_mul_f32 v[152:153], v[122:123], v[156:157]
	v_add_f32_e32 v123, 1.0, v148
	v_add_f32_e32 v122, 1.0, v154
	v_rcp_f32_e32 v148, v123
	v_add_f32_e32 v123, 1.0, v155
	v_rcp_f32_e32 v122, v122
	v_rcp_f32_e32 v123, v123
	s_nop 0
	v_pk_mul_f32 v[128:129], v[128:129], v[122:123]
	v_add_f32_e32 v122, 1.0, v149
	v_rcp_f32_e32 v149, v122
	v_cvt_pk_bf16_f32 v122, v126, v127
	v_cvt_pk_bf16_f32 v123, v128, v129
	v_cvt_pk_f32_fp8_e32 v[126:127], v151
	v_pk_mul_f32 v[148:149], v[124:125], v[148:149]
	v_cvt_pk_bf16_f32 v124, v152, v153
	v_cvt_pk_bf16_f32 v125, v148, v149
	global_store_dwordx4 v[144:145], v[122:125], off
	v_add_f32_e32 v126, 1.0, v126
	v_cvt_pk_f32_fp8_sdwa v[128:129], v151 src0_sel:WORD_1
	v_cvt_pk_f32_fp8_e32 v[122:123], v150
	v_rcp_f32_e32 v126, v126
	v_cvt_pk_f32_fp8_sdwa v[124:125], v150 src0_sel:WORD_1
	v_add_f32_e32 v122, 1.0, v122
	v_add_f32_e32 v123, 1.0, v123
	v_rcp_f32_e32 v122, v122
	v_rcp_f32_e32 v123, v123
	s_nop 0
	v_pk_mul_f32 v[118:119], v[118:119], v[122:123]
	v_add_f32_e32 v122, 1.0, v127
	v_rcp_f32_e32 v127, v122
	s_nop 0
	v_pk_mul_f32 v[122:123], v[114:115], v[126:127]
	v_add_f32_e32 v115, 1.0, v128
	v_add_f32_e32 v114, 1.0, v124
	v_rcp_f32_e32 v124, v115
	v_add_f32_e32 v115, 1.0, v125
	v_rcp_f32_e32 v114, v114
	v_rcp_f32_e32 v115, v115
	s_nop 0
	v_pk_mul_f32 v[120:121], v[120:121], v[114:115]
	v_add_f32_e32 v114, 1.0, v129
	v_rcp_f32_e32 v125, v114
	v_cvt_pk_bf16_f32 v114, v118, v119
	v_cvt_pk_bf16_f32 v115, v120, v121
	v_cvt_pk_f32_fp8_e32 v[118:119], v141
	v_pk_mul_f32 v[124:125], v[116:117], v[124:125]
	v_cvt_pk_bf16_f32 v116, v122, v123
	v_cvt_pk_bf16_f32 v117, v124, v125
	global_store_dwordx4 v[144:145], v[114:117], off offset:16
	v_add_f32_e32 v118, 1.0, v118
	v_cvt_pk_f32_fp8_sdwa v[120:121], v141 src0_sel:WORD_1
	v_cvt_pk_f32_fp8_e32 v[114:115], v140
	v_rcp_f32_e32 v118, v118
	v_cvt_pk_f32_fp8_sdwa v[116:117], v140 src0_sel:WORD_1
	v_add_f32_e32 v114, 1.0, v114
	v_add_f32_e32 v115, 1.0, v115
	v_rcp_f32_e32 v114, v114
	v_rcp_f32_e32 v115, v115
	s_nop 0
	v_pk_mul_f32 v[110:111], v[110:111], v[114:115]
	v_add_f32_e32 v114, 1.0, v119
	v_rcp_f32_e32 v119, v114
	s_nop 0
	v_pk_mul_f32 v[114:115], v[106:107], v[118:119]
	v_add_f32_e32 v107, 1.0, v120
	v_add_f32_e32 v106, 1.0, v116
	v_rcp_f32_e32 v116, v107
	v_add_f32_e32 v107, 1.0, v117
	v_rcp_f32_e32 v106, v106
	v_rcp_f32_e32 v107, v107
	s_nop 0
	v_pk_mul_f32 v[112:113], v[112:113], v[106:107]
	v_add_f32_e32 v106, 1.0, v121
	v_rcp_f32_e32 v117, v106
	v_cvt_pk_bf16_f32 v106, v110, v111
	v_add_co_u32_e32 v110, vcc, s7, v144
	v_pk_mul_f32 v[116:117], v[108:109], v[116:117]
	v_cvt_pk_bf16_f32 v107, v112, v113
	v_cvt_pk_bf16_f32 v108, v114, v115
	v_cvt_pk_bf16_f32 v109, v116, v117
	v_addc_co_u32_e32 v111, vcc, 0, v145, vcc
	global_store_dwordx4 v[110:111], v[106:109], off
	v_cvt_pk_f32_fp8_e32 v[112:113], v143
	v_cvt_pk_f32_fp8_sdwa v[114:115], v143 src0_sel:WORD_1
	v_cvt_pk_f32_fp8_e32 v[106:107], v142
	v_cvt_pk_f32_fp8_sdwa v[108:109], v142 src0_sel:WORD_1
	v_add_f32_e32 v112, 1.0, v112
	v_rcp_f32_e32 v112, v112
	v_add_f32_e32 v106, 1.0, v106
	v_add_f32_e32 v107, 1.0, v107
	v_rcp_f32_e32 v106, v106
	v_rcp_f32_e32 v107, v107
	s_mov_b32 s7, 0x10000
	v_pk_mul_f32 v[102:103], v[102:103], v[106:107]
	v_add_f32_e32 v106, 1.0, v113
	v_rcp_f32_e32 v113, v106
	s_nop 0
	v_pk_mul_f32 v[106:107], v[98:99], v[112:113]
	v_add_f32_e32 v99, 1.0, v114
	v_add_f32_e32 v98, 1.0, v108
	v_rcp_f32_e32 v108, v99
	v_add_f32_e32 v99, 1.0, v109
	v_rcp_f32_e32 v98, v98
	v_rcp_f32_e32 v99, v99
	s_nop 0
	v_pk_mul_f32 v[104:105], v[104:105], v[98:99]
	v_add_f32_e32 v98, 1.0, v115
	v_rcp_f32_e32 v109, v98
	v_cvt_pk_bf16_f32 v98, v102, v103
	v_cvt_pk_bf16_f32 v99, v104, v105
	v_cvt_pk_f32_fp8_e32 v[102:103], v137
	v_pk_mul_f32 v[108:109], v[100:101], v[108:109]
	v_cvt_pk_bf16_f32 v100, v106, v107
	v_cvt_pk_bf16_f32 v101, v108, v109
	global_store_dwordx4 v[110:111], v[98:101], off offset:16
	v_add_f32_e32 v102, 1.0, v102
	v_cvt_pk_f32_fp8_sdwa v[104:105], v137 src0_sel:WORD_1
	v_cvt_pk_f32_fp8_e32 v[98:99], v136
	v_rcp_f32_e32 v102, v102
	v_cvt_pk_f32_fp8_sdwa v[100:101], v136 src0_sel:WORD_1
	v_add_f32_e32 v98, 1.0, v98
	v_add_f32_e32 v99, 1.0, v99
	v_rcp_f32_e32 v98, v98
	v_rcp_f32_e32 v99, v99
	s_nop 0
	v_pk_mul_f32 v[94:95], v[94:95], v[98:99]
	v_add_f32_e32 v98, 1.0, v103
	v_rcp_f32_e32 v103, v98
	s_nop 0
	v_pk_mul_f32 v[98:99], v[90:91], v[102:103]
	v_add_f32_e32 v91, 1.0, v104
	v_add_f32_e32 v90, 1.0, v100
	v_rcp_f32_e32 v100, v91
	v_add_f32_e32 v91, 1.0, v101
	v_rcp_f32_e32 v90, v90
	v_rcp_f32_e32 v91, v91
	s_nop 0
	v_pk_mul_f32 v[96:97], v[96:97], v[90:91]
	v_add_f32_e32 v90, 1.0, v105
	v_rcp_f32_e32 v101, v90
	v_cvt_pk_bf16_f32 v90, v94, v95
	v_add_co_u32_e32 v94, vcc, s7, v144
	v_pk_mul_f32 v[100:101], v[92:93], v[100:101]
	v_cvt_pk_bf16_f32 v91, v96, v97
	v_cvt_pk_bf16_f32 v92, v98, v99
	v_cvt_pk_bf16_f32 v93, v100, v101
	v_addc_co_u32_e32 v95, vcc, 0, v145, vcc
	global_store_dwordx4 v[94:95], v[90:93], off
	v_cvt_pk_f32_fp8_e32 v[96:97], v139
	v_cvt_pk_f32_fp8_sdwa v[98:99], v139 src0_sel:WORD_1
	v_cvt_pk_f32_fp8_e32 v[90:91], v138
	v_cvt_pk_f32_fp8_sdwa v[92:93], v138 src0_sel:WORD_1
	v_add_f32_e32 v96, 1.0, v96
	v_rcp_f32_e32 v96, v96
	v_add_f32_e32 v90, 1.0, v90
	v_add_f32_e32 v91, 1.0, v91
	v_rcp_f32_e32 v90, v90
	v_rcp_f32_e32 v91, v91
	s_mov_b32 s7, 0x18000
	v_pk_mul_f32 v[86:87], v[86:87], v[90:91]
	v_add_f32_e32 v90, 1.0, v97
	v_rcp_f32_e32 v97, v90
	s_nop 0
	v_pk_mul_f32 v[90:91], v[82:83], v[96:97]
	v_add_f32_e32 v83, 1.0, v98
	v_add_f32_e32 v82, 1.0, v92
	v_rcp_f32_e32 v92, v83
	v_add_f32_e32 v83, 1.0, v93
	v_rcp_f32_e32 v82, v82
	v_rcp_f32_e32 v83, v83
	s_nop 0
	v_pk_mul_f32 v[88:89], v[88:89], v[82:83]
	v_add_f32_e32 v82, 1.0, v99
	v_rcp_f32_e32 v93, v82
	v_cvt_pk_bf16_f32 v82, v86, v87
	v_cvt_pk_bf16_f32 v83, v88, v89
	v_cvt_pk_f32_fp8_e32 v[86:87], v133
	v_pk_mul_f32 v[92:93], v[84:85], v[92:93]
	v_cvt_pk_bf16_f32 v84, v90, v91
	v_cvt_pk_bf16_f32 v85, v92, v93
	global_store_dwordx4 v[94:95], v[82:85], off offset:16
	v_add_f32_e32 v86, 1.0, v86
	v_cvt_pk_f32_fp8_sdwa v[88:89], v133 src0_sel:WORD_1
	v_cvt_pk_f32_fp8_e32 v[82:83], v132
	v_rcp_f32_e32 v86, v86
	v_cvt_pk_f32_fp8_sdwa v[84:85], v132 src0_sel:WORD_1
	v_add_f32_e32 v82, 1.0, v82
	v_add_f32_e32 v83, 1.0, v83
	v_rcp_f32_e32 v82, v82
	v_rcp_f32_e32 v83, v83
	s_nop 0
	v_pk_mul_f32 v[78:79], v[78:79], v[82:83]
	v_add_f32_e32 v82, 1.0, v87
	v_rcp_f32_e32 v87, v82
	s_nop 0
	v_pk_mul_f32 v[82:83], v[74:75], v[86:87]
	v_add_f32_e32 v75, 1.0, v88
	v_add_f32_e32 v74, 1.0, v84
	v_rcp_f32_e32 v84, v75
	v_add_f32_e32 v75, 1.0, v85
	v_rcp_f32_e32 v74, v74
	v_rcp_f32_e32 v75, v75
	s_nop 0
	v_pk_mul_f32 v[80:81], v[80:81], v[74:75]
	v_add_f32_e32 v74, 1.0, v89
	v_rcp_f32_e32 v85, v74
	v_cvt_pk_bf16_f32 v74, v78, v79
	v_add_co_u32_e32 v78, vcc, s7, v144
	v_pk_mul_f32 v[84:85], v[76:77], v[84:85]
	v_cvt_pk_bf16_f32 v75, v80, v81
	v_cvt_pk_bf16_f32 v76, v82, v83
	v_cvt_pk_bf16_f32 v77, v84, v85
	v_addc_co_u32_e32 v79, vcc, 0, v145, vcc
	global_store_dwordx4 v[78:79], v[74:77], off
	v_cvt_pk_f32_fp8_e32 v[80:81], v135
	v_cvt_pk_f32_fp8_sdwa v[82:83], v135 src0_sel:WORD_1
	v_cvt_pk_f32_fp8_e32 v[74:75], v134
	v_cvt_pk_f32_fp8_sdwa v[76:77], v134 src0_sel:WORD_1
	v_add_f32_e32 v80, 1.0, v80
	v_rcp_f32_e32 v80, v80
	v_add_f32_e32 v74, 1.0, v74
	v_add_f32_e32 v75, 1.0, v75
	v_rcp_f32_e32 v74, v74
	v_rcp_f32_e32 v75, v75
	s_mov_b32 s7, 0xf0000
	v_pk_mul_f32 v[70:71], v[70:71], v[74:75]
	v_add_f32_e32 v74, 1.0, v81
	v_rcp_f32_e32 v81, v74
	s_nop 0
	v_pk_mul_f32 v[74:75], v[66:67], v[80:81]
	v_add_f32_e32 v67, 1.0, v82
	v_add_f32_e32 v66, 1.0, v76
	v_rcp_f32_e32 v76, v67
	v_add_f32_e32 v67, 1.0, v77
	v_rcp_f32_e32 v66, v66
	v_rcp_f32_e32 v67, v67
	s_nop 0
	v_pk_mul_f32 v[72:73], v[72:73], v[66:67]
	v_add_f32_e32 v66, 1.0, v83
	v_rcp_f32_e32 v77, v66
	v_cvt_pk_bf16_f32 v66, v70, v71
	v_cvt_pk_bf16_f32 v67, v72, v73
	v_pk_mul_f32 v[76:77], v[68:69], v[76:77]
	v_cvt_pk_bf16_f32 v68, v74, v75
	v_cvt_pk_bf16_f32 v69, v76, v77
	global_store_dwordx4 v[78:79], v[66:69], off offset:16
	s_nop 1
	v_add_co_u32_e32 v66, vcc, s7, v146
	s_mov_b32 s7, 0x10e000
	s_nop 0
	v_addc_co_u32_e32 v67, vcc, 0, v147, vcc
	global_load_dwordx4 v[74:77], v[66:67], off offset:3584 nt
	v_add_co_u32_e32 v66, vcc, s7, v146
	s_mov_b32 s7, 0x12c000
	s_nop 0
	v_addc_co_u32_e32 v67, vcc, 0, v147, vcc
	global_load_dwordx4 v[78:81], v[66:67], off offset:3584 nt
	v_add_co_u32_e32 v66, vcc, s7, v146
	s_mov_b32 s7, 0x14a000
	s_nop 0
	v_addc_co_u32_e32 v67, vcc, 0, v147, vcc
	global_load_dwordx4 v[70:73], v[66:67], off offset:3584 nt
	v_add_co_u32_e32 v66, vcc, s7, v146
	s_mov_b32 s7, 0x40000
	s_nop 0
	v_addc_co_u32_e32 v67, vcc, 0, v147, vcc
	global_load_dwordx4 v[66:69], v[66:67], off offset:3584 nt
	s_waitcnt vmcnt(0)
	v_cvt_pk_f32_fp8_e32 v[82:83], v74
	v_cvt_pk_f32_fp8_e32 v[86:87], v75
	v_cvt_pk_f32_fp8_sdwa v[84:85], v74 src0_sel:WORD_1
	v_cvt_pk_f32_fp8_sdwa v[74:75], v75 src0_sel:WORD_1
	v_add_f32_e32 v82, 1.0, v82
	v_add_f32_e32 v83, 1.0, v83
	v_rcp_f32_e32 v82, v82
	v_rcp_f32_e32 v83, v83
	v_add_f32_e32 v86, 1.0, v86
	v_rcp_f32_e32 v86, v86
	v_pk_mul_f32 v[62:63], v[62:63], v[82:83]
	v_add_f32_e32 v82, 1.0, v87
	v_rcp_f32_e32 v87, v82
	s_nop 0
	v_pk_mul_f32 v[82:83], v[58:59], v[86:87]
	v_add_f32_e32 v59, 1.0, v74
	v_add_f32_e32 v58, 1.0, v84
	v_rcp_f32_e32 v74, v59
	v_add_f32_e32 v59, 1.0, v85
	v_rcp_f32_e32 v58, v58
	v_rcp_f32_e32 v59, v59
	s_nop 0
	v_pk_mul_f32 v[64:65], v[64:65], v[58:59]
	v_add_f32_e32 v58, 1.0, v75
	v_rcp_f32_e32 v75, v58
	v_cvt_pk_bf16_f32 v58, v62, v63
	v_add_co_u32_e32 v62, vcc, s7, v144
	v_pk_mul_f32 v[74:75], v[60:61], v[74:75]
	v_cvt_pk_bf16_f32 v59, v64, v65
	v_cvt_pk_bf16_f32 v60, v82, v83
	v_cvt_pk_bf16_f32 v61, v74, v75
	v_addc_co_u32_e32 v63, vcc, 0, v145, vcc
	global_store_dwordx4 v[62:63], v[58:61], off
	v_cvt_pk_f32_fp8_e32 v[64:65], v77
	v_cvt_pk_f32_fp8_sdwa v[74:75], v77 src0_sel:WORD_1
	v_cvt_pk_f32_fp8_e32 v[58:59], v76
	v_cvt_pk_f32_fp8_sdwa v[60:61], v76 src0_sel:WORD_1
	v_add_f32_e32 v64, 1.0, v64
	v_rcp_f32_e32 v64, v64
	v_add_f32_e32 v58, 1.0, v58
	v_add_f32_e32 v59, 1.0, v59
	v_rcp_f32_e32 v58, v58
	v_rcp_f32_e32 v59, v59
	s_mov_b32 s7, 0x48000
	v_pk_mul_f32 v[54:55], v[54:55], v[58:59]
	v_add_f32_e32 v58, 1.0, v65
	v_rcp_f32_e32 v65, v58
	s_nop 0
	v_pk_mul_f32 v[58:59], v[50:51], v[64:65]
	v_add_f32_e32 v51, 1.0, v74
	v_add_f32_e32 v50, 1.0, v60
	v_rcp_f32_e32 v60, v51
	v_add_f32_e32 v51, 1.0, v61
	v_rcp_f32_e32 v50, v50
	v_rcp_f32_e32 v51, v51
	s_nop 0
	v_pk_mul_f32 v[56:57], v[56:57], v[50:51]
	v_add_f32_e32 v50, 1.0, v75
	v_rcp_f32_e32 v61, v50
	v_cvt_pk_bf16_f32 v50, v54, v55
	v_cvt_pk_bf16_f32 v51, v56, v57
	v_cvt_pk_f32_fp8_e32 v[54:55], v79
	v_pk_mul_f32 v[60:61], v[52:53], v[60:61]
	v_cvt_pk_bf16_f32 v52, v58, v59
	v_cvt_pk_bf16_f32 v53, v60, v61
	global_store_dwordx4 v[62:63], v[50:53], off offset:16
	v_add_f32_e32 v54, 1.0, v54
	v_cvt_pk_f32_fp8_sdwa v[56:57], v79 src0_sel:WORD_1
	v_cvt_pk_f32_fp8_e32 v[50:51], v78
	v_rcp_f32_e32 v54, v54
	v_cvt_pk_f32_fp8_sdwa v[52:53], v78 src0_sel:WORD_1
	v_add_f32_e32 v50, 1.0, v50
	v_add_f32_e32 v51, 1.0, v51
	v_rcp_f32_e32 v50, v50
	v_rcp_f32_e32 v51, v51
	s_nop 0
	v_pk_mul_f32 v[46:47], v[46:47], v[50:51]
	v_add_f32_e32 v50, 1.0, v55
	v_rcp_f32_e32 v55, v50
	s_nop 0
	v_pk_mul_f32 v[50:51], v[42:43], v[54:55]
	v_add_f32_e32 v43, 1.0, v56
	v_add_f32_e32 v42, 1.0, v52
	v_rcp_f32_e32 v52, v43
	v_add_f32_e32 v43, 1.0, v53
	v_rcp_f32_e32 v42, v42
	v_rcp_f32_e32 v43, v43
	s_nop 0
	v_pk_mul_f32 v[48:49], v[48:49], v[42:43]
	v_add_f32_e32 v42, 1.0, v57
	v_rcp_f32_e32 v53, v42
	v_cvt_pk_bf16_f32 v42, v46, v47
	v_add_co_u32_e32 v46, vcc, s7, v144
	v_pk_mul_f32 v[52:53], v[44:45], v[52:53]
	v_cvt_pk_bf16_f32 v43, v48, v49
	v_cvt_pk_bf16_f32 v44, v50, v51
	v_cvt_pk_bf16_f32 v45, v52, v53
	v_addc_co_u32_e32 v47, vcc, 0, v145, vcc
	global_store_dwordx4 v[46:47], v[42:45], off
	v_cvt_pk_f32_fp8_e32 v[48:49], v81
	v_cvt_pk_f32_fp8_sdwa v[50:51], v81 src0_sel:WORD_1
	v_cvt_pk_f32_fp8_e32 v[42:43], v80
	v_cvt_pk_f32_fp8_sdwa v[44:45], v80 src0_sel:WORD_1
	v_add_f32_e32 v48, 1.0, v48
	v_rcp_f32_e32 v48, v48
	v_add_f32_e32 v42, 1.0, v42
	v_add_f32_e32 v43, 1.0, v43
	v_rcp_f32_e32 v42, v42
	v_rcp_f32_e32 v43, v43
	s_mov_b32 s7, 0x50000
	v_pk_mul_f32 v[38:39], v[38:39], v[42:43]
	v_add_f32_e32 v42, 1.0, v49
	v_rcp_f32_e32 v49, v42
	s_nop 0
	v_pk_mul_f32 v[42:43], v[34:35], v[48:49]
	v_add_f32_e32 v35, 1.0, v50
	v_add_f32_e32 v34, 1.0, v44
	v_rcp_f32_e32 v44, v35
	v_add_f32_e32 v35, 1.0, v45
	v_rcp_f32_e32 v34, v34
	v_rcp_f32_e32 v35, v35
	s_nop 0
	v_pk_mul_f32 v[40:41], v[40:41], v[34:35]
	v_add_f32_e32 v34, 1.0, v51
	v_rcp_f32_e32 v45, v34
	v_cvt_pk_bf16_f32 v34, v38, v39
	v_cvt_pk_bf16_f32 v35, v40, v41
	v_cvt_pk_f32_fp8_e32 v[38:39], v71
	v_pk_mul_f32 v[44:45], v[36:37], v[44:45]
	v_cvt_pk_bf16_f32 v36, v42, v43
	v_cvt_pk_bf16_f32 v37, v44, v45
	global_store_dwordx4 v[46:47], v[34:37], off offset:16
	v_add_f32_e32 v38, 1.0, v38
	v_cvt_pk_f32_fp8_sdwa v[40:41], v71 src0_sel:WORD_1
	v_cvt_pk_f32_fp8_e32 v[34:35], v70
	v_rcp_f32_e32 v38, v38
	v_cvt_pk_f32_fp8_sdwa v[36:37], v70 src0_sel:WORD_1
	v_add_f32_e32 v34, 1.0, v34
	v_add_f32_e32 v35, 1.0, v35
	v_rcp_f32_e32 v34, v34
	v_rcp_f32_e32 v35, v35
	s_nop 0
	v_pk_mul_f32 v[30:31], v[30:31], v[34:35]
	v_add_f32_e32 v34, 1.0, v39
	v_rcp_f32_e32 v39, v34
	s_nop 0
	v_pk_mul_f32 v[34:35], v[26:27], v[38:39]
	v_add_f32_e32 v27, 1.0, v40
	v_add_f32_e32 v26, 1.0, v36
	v_rcp_f32_e32 v36, v27
	v_add_f32_e32 v27, 1.0, v37
	v_rcp_f32_e32 v26, v26
	v_rcp_f32_e32 v27, v27
	s_nop 0
	v_pk_mul_f32 v[32:33], v[32:33], v[26:27]
	v_add_f32_e32 v26, 1.0, v41
	v_rcp_f32_e32 v37, v26
	v_cvt_pk_bf16_f32 v26, v30, v31
	v_add_co_u32_e32 v30, vcc, s7, v144
	v_pk_mul_f32 v[36:37], v[28:29], v[36:37]
	v_cvt_pk_bf16_f32 v27, v32, v33
	v_cvt_pk_bf16_f32 v28, v34, v35
	v_cvt_pk_bf16_f32 v29, v36, v37
	v_addc_co_u32_e32 v31, vcc, 0, v145, vcc
	global_store_dwordx4 v[30:31], v[26:29], off
	v_cvt_pk_f32_fp8_e32 v[32:33], v73
	v_cvt_pk_f32_fp8_sdwa v[34:35], v73 src0_sel:WORD_1
	v_cvt_pk_f32_fp8_e32 v[26:27], v72
	v_cvt_pk_f32_fp8_sdwa v[28:29], v72 src0_sel:WORD_1
	v_add_f32_e32 v32, 1.0, v32
	v_rcp_f32_e32 v32, v32
	v_add_f32_e32 v26, 1.0, v26
	v_add_f32_e32 v27, 1.0, v27
	v_rcp_f32_e32 v26, v26
	v_rcp_f32_e32 v27, v27
	s_mov_b32 s7, 0x58000
	v_pk_mul_f32 v[22:23], v[22:23], v[26:27]
	v_add_f32_e32 v26, 1.0, v33
	v_rcp_f32_e32 v33, v26
	s_nop 0
	v_pk_mul_f32 v[26:27], v[18:19], v[32:33]
	v_add_f32_e32 v19, 1.0, v34
	v_add_f32_e32 v18, 1.0, v28
	v_rcp_f32_e32 v28, v19
	v_add_f32_e32 v19, 1.0, v29
	v_rcp_f32_e32 v18, v18
	v_rcp_f32_e32 v19, v19
	s_nop 0
	v_pk_mul_f32 v[24:25], v[24:25], v[18:19]
	v_add_f32_e32 v18, 1.0, v35
	v_rcp_f32_e32 v29, v18
	v_cvt_pk_bf16_f32 v18, v22, v23
	v_cvt_pk_bf16_f32 v19, v24, v25
	v_cvt_pk_f32_fp8_e32 v[22:23], v67
	v_pk_mul_f32 v[28:29], v[20:21], v[28:29]
	v_cvt_pk_bf16_f32 v20, v26, v27
	v_cvt_pk_bf16_f32 v21, v28, v29
	global_store_dwordx4 v[30:31], v[18:21], off offset:16
	v_add_f32_e32 v22, 1.0, v22
	v_cvt_pk_f32_fp8_sdwa v[24:25], v67 src0_sel:WORD_1
	v_cvt_pk_f32_fp8_e32 v[18:19], v66
	v_rcp_f32_e32 v22, v22
	v_cvt_pk_f32_fp8_sdwa v[20:21], v66 src0_sel:WORD_1
	v_add_f32_e32 v18, 1.0, v18
	v_add_f32_e32 v19, 1.0, v19
	v_rcp_f32_e32 v18, v18
	v_rcp_f32_e32 v19, v19
	s_nop 0
	v_pk_mul_f32 v[14:15], v[14:15], v[18:19]
	v_add_f32_e32 v18, 1.0, v23
	v_rcp_f32_e32 v23, v18
	s_nop 0
	v_pk_mul_f32 v[18:19], v[10:11], v[22:23]
	v_add_f32_e32 v11, 1.0, v24
	v_add_f32_e32 v10, 1.0, v20
	v_rcp_f32_e32 v20, v11
	v_add_f32_e32 v11, 1.0, v21
	v_rcp_f32_e32 v10, v10
	v_rcp_f32_e32 v11, v11
	s_nop 0
	v_pk_mul_f32 v[16:17], v[16:17], v[10:11]
	v_add_f32_e32 v10, 1.0, v25
	v_rcp_f32_e32 v21, v10
	v_cvt_pk_bf16_f32 v10, v14, v15
	v_add_co_u32_e32 v14, vcc, s7, v144
	v_pk_mul_f32 v[20:21], v[12:13], v[20:21]
	v_cvt_pk_bf16_f32 v11, v16, v17
	v_cvt_pk_bf16_f32 v12, v18, v19
	v_cvt_pk_bf16_f32 v13, v20, v21
	v_addc_co_u32_e32 v15, vcc, 0, v145, vcc
	global_store_dwordx4 v[14:15], v[10:13], off
	v_cvt_pk_f32_fp8_e32 v[16:17], v69
	v_cvt_pk_f32_fp8_sdwa v[18:19], v69 src0_sel:WORD_1
	v_cvt_pk_f32_fp8_e32 v[10:11], v68
	v_cvt_pk_f32_fp8_sdwa v[12:13], v68 src0_sel:WORD_1
	v_add_f32_e32 v16, 1.0, v16
	v_rcp_f32_e32 v16, v16
	v_add_f32_e32 v10, 1.0, v10
	v_add_f32_e32 v11, 1.0, v11
	v_rcp_f32_e32 v10, v10
	v_rcp_f32_e32 v11, v11
	s_and_b64 vcc, exec, s[4:5]
	v_pk_mul_f32 v[6:7], v[6:7], v[10:11]
	v_add_f32_e32 v10, 1.0, v17
	v_rcp_f32_e32 v17, v10
	s_nop 0
	v_pk_mul_f32 v[10:11], v[2:3], v[16:17]
	v_add_f32_e32 v3, 1.0, v18
	v_add_f32_e32 v2, 1.0, v12
	v_rcp_f32_e32 v12, v3
	v_add_f32_e32 v3, 1.0, v13
	v_rcp_f32_e32 v2, v2
	v_rcp_f32_e32 v3, v3
	s_nop 0
	v_pk_mul_f32 v[8:9], v[8:9], v[2:3]
	v_add_f32_e32 v2, 1.0, v19
	v_rcp_f32_e32 v13, v2
	v_cvt_pk_bf16_f32 v2, v6, v7
	v_cvt_pk_bf16_f32 v3, v8, v9
	v_pk_mul_f32 v[12:13], v[4:5], v[12:13]
	v_cvt_pk_bf16_f32 v4, v10, v11
	v_cvt_pk_bf16_f32 v5, v12, v13
	global_store_dwordx4 v[14:15], v[2:5], off offset:16
	s_cbranch_vccnz .LBB0_1106

.LBB0_1104:
	s_add_i32 s57, s57, 2
	s_and_b32 s58, s57, 10
	s_cmp_lg_u32 s58, 8
	s_cbranch_scc1 .LBB0_1103
	s_cmpk_eq_i32 s62, 0x400
	s_cselect_b32 s58, 0, 0x400
	s_add_u32 s64, s14, s58
	v_mov_b32_e32 v130, v183
	s_addc_u32 s65, s15, 0
	global_load_dwordx4 v[156:159], v130, s[64:65] offset:1536 nt
	global_load_dwordx4 v[160:163], v130, s[64:65] offset:2560 nt
	v_add_u32_e32 v132, 0x1e000, v130
	global_load_dwordx4 v[148:151], v132, s[64:65] offset:1536 nt
	global_load_dwordx4 v[152:155], v132, s[64:65] offset:2560 nt
	v_add_u32_e32 v132, 0x3c000, v130
	global_load_dwordx4 v[144:147], v132, s[64:65] offset:1536 nt
	global_load_dwordx4 v[140:143], v132, s[64:65] offset:2560 nt
	v_add_u32_e32 v136, 0x5a000, v130
	global_load_dwordx4 v[132:135], v136, s[64:65] offset:1536 nt
	s_nop 0
	global_load_dwordx4 v[136:139], v136, s[64:65] offset:2560 nt
	s_waitcnt vmcnt(0)
	v_cvt_pk_f32_fp8_e32 v[186:187], v156
	v_cvt_pk_f32_fp8_sdwa v[188:189], v156 src0_sel:WORD_1
	v_cvt_pk_f32_fp8_e32 v[190:191], v160
	v_cvt_pk_f32_fp8_sdwa v[192:193], v160 src0_sel:WORD_1
	v_add_f32_e32 v156, 1.0, v186
	v_rcp_f32_e32 v186, v156
	v_add_f32_e32 v156, 1.0, v187
	v_rcp_f32_e32 v187, v156
	v_add_f32_e32 v156, 1.0, v188
	v_rcp_f32_e32 v188, v156
	v_add_f32_e32 v156, 1.0, v189
	v_pk_add_f32 v[190:191], v[190:191], 1.0 op_sel_hi:[1,0]
	v_rcp_f32_e32 v189, v156
	v_pk_mul_f32 v[186:187], v[186:187], v[190:191]
	v_pk_add_f32 v[192:193], v[192:193], 1.0 op_sel_hi:[1,0]
	v_pk_mul_f32 v[126:127], v[126:127], v[186:187]
	v_cvt_pk_f32_fp8_e32 v[186:187], v157
	v_cvt_pk_f32_fp8_sdwa v[156:157], v157 src0_sel:WORD_1
	v_pk_mul_f32 v[188:189], v[188:189], v[192:193]
	v_add_f32_e32 v186, 1.0, v186
	v_pk_mul_f32 v[128:129], v[128:129], v[188:189]
	v_cvt_pk_f32_fp8_e32 v[188:189], v161
	v_cvt_pk_f32_fp8_sdwa v[160:161], v161 src0_sel:WORD_1
	v_add_f32_e32 v156, 1.0, v156
	v_add_f32_e32 v157, 1.0, v157
	v_rcp_f32_e32 v156, v156
	v_rcp_f32_e32 v157, v157
	v_add_f32_e32 v187, 1.0, v187
	v_pk_add_f32 v[160:161], v[160:161], 1.0 op_sel_hi:[1,0]
	v_rcp_f32_e32 v186, v186
	v_rcp_f32_e32 v187, v187
	v_pk_mul_f32 v[156:157], v[156:157], v[160:161]
	v_pk_add_f32 v[188:189], v[188:189], 1.0 op_sel_hi:[1,0]
	v_pk_mul_f32 v[124:125], v[124:125], v[156:157]
	v_cvt_pk_f32_fp8_e32 v[156:157], v158
	v_pk_mul_f32 v[186:187], v[186:187], v[188:189]
	v_cvt_pk_f32_fp8_sdwa v[160:161], v158 src0_sel:WORD_1
	v_pk_mul_f32 v[122:123], v[122:123], v[186:187]
	v_cvt_pk_f32_fp8_e32 v[186:187], v162
	v_add_f32_e32 v156, 1.0, v156
	v_add_f32_e32 v157, 1.0, v157
	v_rcp_f32_e32 v156, v156
	v_rcp_f32_e32 v157, v157
	v_add_f32_e32 v158, 1.0, v160
	v_cvt_pk_f32_fp8_sdwa v[188:189], v162 src0_sel:WORD_1
	v_rcp_f32_e32 v160, v158
	v_add_f32_e32 v158, 1.0, v161
	v_pk_add_f32 v[186:187], v[186:187], 1.0 op_sel_hi:[1,0]
	v_rcp_f32_e32 v161, v158
	v_pk_mul_f32 v[156:157], v[156:157], v[186:187]
	v_pk_add_f32 v[188:189], v[188:189], 1.0 op_sel_hi:[1,0]
	v_pk_mul_f32 v[118:119], v[118:119], v[156:157]
	v_cvt_pk_f32_fp8_e32 v[156:157], v159
	v_pk_mul_f32 v[160:161], v[160:161], v[188:189]
	v_cvt_pk_f32_fp8_sdwa v[158:159], v159 src0_sel:WORD_1
	v_pk_mul_f32 v[120:121], v[120:121], v[160:161]
	v_cvt_pk_f32_fp8_e32 v[160:161], v163
	v_add_f32_e32 v156, 1.0, v156
	v_add_f32_e32 v157, 1.0, v157
	v_rcp_f32_e32 v156, v156
	v_rcp_f32_e32 v157, v157
	v_cvt_pk_f32_fp8_sdwa v[162:163], v163 src0_sel:WORD_1
	v_add_f32_e32 v158, 1.0, v158
	v_add_f32_e32 v159, 1.0, v159
	v_pk_add_f32 v[160:161], v[160:161], 1.0 op_sel_hi:[1,0]
	v_rcp_f32_e32 v158, v158
	v_rcp_f32_e32 v159, v159
	v_pk_mul_f32 v[156:157], v[156:157], v[160:161]
	v_pk_add_f32 v[162:163], v[162:163], 1.0 op_sel_hi:[1,0]
	v_pk_mul_f32 v[114:115], v[114:115], v[156:157]
	v_cvt_pk_f32_fp8_e32 v[156:157], v148
	v_pk_mul_f32 v[158:159], v[158:159], v[162:163]
	v_cvt_pk_f32_fp8_e32 v[160:161], v152
	v_pk_mul_f32 v[116:117], v[116:117], v[158:159]
	v_cvt_pk_f32_fp8_sdwa v[158:159], v148 src0_sel:WORD_1
	v_add_f32_e32 v148, 1.0, v156
	v_rcp_f32_e32 v156, v148
	v_add_f32_e32 v148, 1.0, v157
	v_rcp_f32_e32 v157, v148
	v_add_f32_e32 v148, 1.0, v158
	v_cvt_pk_f32_fp8_sdwa v[162:163], v152 src0_sel:WORD_1
	v_rcp_f32_e32 v158, v148
	v_add_f32_e32 v148, 1.0, v159
	v_pk_add_f32 v[160:161], v[160:161], 1.0 op_sel_hi:[1,0]
	v_rcp_f32_e32 v159, v148
	v_pk_mul_f32 v[156:157], v[156:157], v[160:161]
	v_pk_add_f32 v[162:163], v[162:163], 1.0 op_sel_hi:[1,0]
	v_pk_mul_f32 v[110:111], v[110:111], v[156:157]
	v_cvt_pk_f32_fp8_e32 v[156:157], v149
	v_cvt_pk_f32_fp8_sdwa v[148:149], v149 src0_sel:WORD_1
	v_pk_mul_f32 v[158:159], v[158:159], v[162:163]
	v_add_f32_e32 v156, 1.0, v156
	v_pk_mul_f32 v[112:113], v[112:113], v[158:159]
	v_cvt_pk_f32_fp8_e32 v[158:159], v153
	v_cvt_pk_f32_fp8_sdwa v[152:153], v153 src0_sel:WORD_1
	v_add_f32_e32 v148, 1.0, v148
	v_add_f32_e32 v149, 1.0, v149
	v_rcp_f32_e32 v148, v148
	v_rcp_f32_e32 v149, v149
	v_add_f32_e32 v157, 1.0, v157
	v_pk_add_f32 v[152:153], v[152:153], 1.0 op_sel_hi:[1,0]
	v_rcp_f32_e32 v156, v156
	v_rcp_f32_e32 v157, v157
	v_pk_mul_f32 v[148:149], v[148:149], v[152:153]
	v_pk_add_f32 v[158:159], v[158:159], 1.0 op_sel_hi:[1,0]
	v_pk_mul_f32 v[108:109], v[108:109], v[148:149]
	v_cvt_pk_f32_fp8_e32 v[148:149], v150
	v_pk_mul_f32 v[156:157], v[156:157], v[158:159]
	v_cvt_pk_f32_fp8_sdwa v[152:153], v150 src0_sel:WORD_1
	v_pk_mul_f32 v[106:107], v[106:107], v[156:157]
	v_cvt_pk_f32_fp8_e32 v[156:157], v154
	v_add_f32_e32 v148, 1.0, v148
	v_add_f32_e32 v149, 1.0, v149
	v_rcp_f32_e32 v148, v148
	v_rcp_f32_e32 v149, v149
	v_add_f32_e32 v150, 1.0, v152
	v_cvt_pk_f32_fp8_sdwa v[158:159], v154 src0_sel:WORD_1
	v_rcp_f32_e32 v152, v150
	v_add_f32_e32 v150, 1.0, v153
	v_pk_add_f32 v[156:157], v[156:157], 1.0 op_sel_hi:[1,0]
	v_rcp_f32_e32 v153, v150
	v_pk_mul_f32 v[148:149], v[148:149], v[156:157]
	v_pk_add_f32 v[158:159], v[158:159], 1.0 op_sel_hi:[1,0]
	v_pk_mul_f32 v[102:103], v[102:103], v[148:149]
	v_cvt_pk_f32_fp8_e32 v[148:149], v151
	v_pk_mul_f32 v[152:153], v[152:153], v[158:159]
	v_cvt_pk_f32_fp8_sdwa v[150:151], v151 src0_sel:WORD_1
	v_pk_mul_f32 v[104:105], v[104:105], v[152:153]
	v_cvt_pk_f32_fp8_e32 v[152:153], v155
	v_add_f32_e32 v148, 1.0, v148
	v_add_f32_e32 v149, 1.0, v149
	v_rcp_f32_e32 v148, v148
	v_rcp_f32_e32 v149, v149
	v_cvt_pk_f32_fp8_sdwa v[154:155], v155 src0_sel:WORD_1
	v_add_f32_e32 v150, 1.0, v150
	v_add_f32_e32 v151, 1.0, v151
	v_pk_add_f32 v[152:153], v[152:153], 1.0 op_sel_hi:[1,0]
	v_rcp_f32_e32 v150, v150
	v_rcp_f32_e32 v151, v151
	v_pk_mul_f32 v[148:149], v[148:149], v[152:153]
	v_pk_add_f32 v[154:155], v[154:155], 1.0 op_sel_hi:[1,0]
	v_pk_mul_f32 v[98:99], v[98:99], v[148:149]
	v_cvt_pk_f32_fp8_e32 v[148:149], v144
	v_pk_mul_f32 v[150:151], v[150:151], v[154:155]
	v_cvt_pk_f32_fp8_e32 v[152:153], v140
	v_pk_mul_f32 v[100:101], v[100:101], v[150:151]
	v_cvt_pk_f32_fp8_sdwa v[150:151], v144 src0_sel:WORD_1
	v_cvt_pk_f32_fp8_sdwa v[154:155], v140 src0_sel:WORD_1
	v_add_f32_e32 v140, 1.0, v148
	v_rcp_f32_e32 v148, v140
	v_add_f32_e32 v140, 1.0, v149
	v_rcp_f32_e32 v149, v140
	v_add_f32_e32 v140, 1.0, v150
	v_rcp_f32_e32 v150, v140
	v_add_f32_e32 v140, 1.0, v151
	v_pk_add_f32 v[152:153], v[152:153], 1.0 op_sel_hi:[1,0]
	v_rcp_f32_e32 v151, v140
	v_pk_mul_f32 v[148:149], v[148:149], v[152:153]
	v_pk_add_f32 v[154:155], v[154:155], 1.0 op_sel_hi:[1,0]
	v_pk_mul_f32 v[94:95], v[94:95], v[148:149]
	v_cvt_pk_f32_fp8_e32 v[148:149], v145
	v_cvt_pk_f32_fp8_sdwa v[144:145], v145 src0_sel:WORD_1
	v_pk_mul_f32 v[150:151], v[150:151], v[154:155]
	v_add_f32_e32 v148, 1.0, v148
	v_pk_mul_f32 v[96:97], v[96:97], v[150:151]
	v_cvt_pk_f32_fp8_e32 v[150:151], v141
	v_cvt_pk_f32_fp8_sdwa v[140:141], v141 src0_sel:WORD_1
	v_add_f32_e32 v144, 1.0, v144
	v_add_f32_e32 v145, 1.0, v145
	v_rcp_f32_e32 v144, v144
	v_rcp_f32_e32 v145, v145
	v_add_f32_e32 v149, 1.0, v149
	v_pk_add_f32 v[140:141], v[140:141], 1.0 op_sel_hi:[1,0]
	v_rcp_f32_e32 v148, v148
	v_rcp_f32_e32 v149, v149
	v_pk_mul_f32 v[140:141], v[144:145], v[140:141]
	v_pk_add_f32 v[150:151], v[150:151], 1.0 op_sel_hi:[1,0]
	v_pk_mul_f32 v[92:93], v[92:93], v[140:141]
	v_cvt_pk_f32_fp8_e32 v[140:141], v146
	v_pk_mul_f32 v[148:149], v[148:149], v[150:151]
	v_cvt_pk_f32_fp8_sdwa v[144:145], v146 src0_sel:WORD_1
	v_pk_mul_f32 v[90:91], v[90:91], v[148:149]
	v_cvt_pk_f32_fp8_e32 v[148:149], v142
	v_add_f32_e32 v140, 1.0, v140
	v_add_f32_e32 v141, 1.0, v141
	v_rcp_f32_e32 v140, v140
	v_rcp_f32_e32 v141, v141
	v_cvt_pk_f32_fp8_sdwa v[150:151], v142 src0_sel:WORD_1
	v_add_f32_e32 v142, 1.0, v144
	v_rcp_f32_e32 v144, v142
	v_add_f32_e32 v142, 1.0, v145
	v_pk_add_f32 v[148:149], v[148:149], 1.0 op_sel_hi:[1,0]
	v_rcp_f32_e32 v145, v142
	v_pk_mul_f32 v[140:141], v[140:141], v[148:149]
	v_pk_add_f32 v[150:151], v[150:151], 1.0 op_sel_hi:[1,0]
	v_pk_mul_f32 v[86:87], v[86:87], v[140:141]
	v_cvt_pk_f32_fp8_e32 v[140:141], v147
	v_pk_mul_f32 v[144:145], v[144:145], v[150:151]
	v_add_f32_e32 v140, 1.0, v140
	v_pk_mul_f32 v[88:89], v[88:89], v[144:145]
	v_cvt_pk_f32_fp8_sdwa v[144:145], v147 src0_sel:WORD_1
	v_cvt_pk_f32_fp8_e32 v[146:147], v143
	v_add_f32_e32 v141, 1.0, v141
	v_rcp_f32_e32 v140, v140
	v_rcp_f32_e32 v141, v141
	v_cvt_pk_f32_fp8_sdwa v[142:143], v143 src0_sel:WORD_1
	v_add_f32_e32 v144, 1.0, v144
	v_add_f32_e32 v145, 1.0, v145
	v_pk_add_f32 v[146:147], v[146:147], 1.0 op_sel_hi:[1,0]
	v_rcp_f32_e32 v144, v144
	v_rcp_f32_e32 v145, v145
	v_pk_mul_f32 v[140:141], v[140:141], v[146:147]
	v_pk_add_f32 v[142:143], v[142:143], 1.0 op_sel_hi:[1,0]
	v_pk_mul_f32 v[82:83], v[82:83], v[140:141]
	v_cvt_pk_f32_fp8_e32 v[140:141], v132
	v_pk_mul_f32 v[142:143], v[144:145], v[142:143]
	v_cvt_pk_f32_fp8_e32 v[144:145], v136
	v_pk_mul_f32 v[84:85], v[84:85], v[142:143]
	v_cvt_pk_f32_fp8_sdwa v[142:143], v132 src0_sel:WORD_1
	v_add_f32_e32 v132, 1.0, v140
	v_rcp_f32_e32 v140, v132
	v_add_f32_e32 v132, 1.0, v141
	v_rcp_f32_e32 v141, v132
	v_add_f32_e32 v132, 1.0, v142
	v_cvt_pk_f32_fp8_sdwa v[146:147], v136 src0_sel:WORD_1
	v_rcp_f32_e32 v142, v132
	v_add_f32_e32 v132, 1.0, v143
	v_pk_add_f32 v[144:145], v[144:145], 1.0 op_sel_hi:[1,0]
	v_rcp_f32_e32 v143, v132
	v_pk_mul_f32 v[140:141], v[140:141], v[144:145]
	v_pk_add_f32 v[146:147], v[146:147], 1.0 op_sel_hi:[1,0]
	v_pk_mul_f32 v[78:79], v[78:79], v[140:141]
	v_cvt_pk_f32_fp8_e32 v[140:141], v133
	v_cvt_pk_f32_fp8_sdwa v[132:133], v133 src0_sel:WORD_1
	v_pk_mul_f32 v[142:143], v[142:143], v[146:147]
	v_add_f32_e32 v140, 1.0, v140
	v_pk_mul_f32 v[80:81], v[80:81], v[142:143]
	v_cvt_pk_f32_fp8_e32 v[142:143], v137
	v_cvt_pk_f32_fp8_sdwa v[136:137], v137 src0_sel:WORD_1
	v_add_f32_e32 v132, 1.0, v132
	v_add_f32_e32 v133, 1.0, v133
	v_rcp_f32_e32 v132, v132
	v_rcp_f32_e32 v133, v133
	v_add_f32_e32 v141, 1.0, v141
	v_pk_add_f32 v[136:137], v[136:137], 1.0 op_sel_hi:[1,0]
	v_rcp_f32_e32 v140, v140
	v_rcp_f32_e32 v141, v141
	v_pk_mul_f32 v[132:133], v[132:133], v[136:137]
	v_pk_add_f32 v[142:143], v[142:143], 1.0 op_sel_hi:[1,0]
	v_pk_mul_f32 v[76:77], v[76:77], v[132:133]
	v_cvt_pk_f32_fp8_e32 v[132:133], v134
	v_pk_mul_f32 v[140:141], v[140:141], v[142:143]
	v_cvt_pk_f32_fp8_sdwa v[136:137], v134 src0_sel:WORD_1
	v_pk_mul_f32 v[74:75], v[74:75], v[140:141]
	v_cvt_pk_f32_fp8_e32 v[140:141], v138
	v_add_f32_e32 v132, 1.0, v132
	v_add_f32_e32 v133, 1.0, v133
	v_rcp_f32_e32 v132, v132
	v_rcp_f32_e32 v133, v133
	v_add_f32_e32 v134, 1.0, v136
	v_cvt_pk_f32_fp8_sdwa v[142:143], v138 src0_sel:WORD_1
	v_rcp_f32_e32 v136, v134
	v_add_f32_e32 v134, 1.0, v137
	v_pk_add_f32 v[140:141], v[140:141], 1.0 op_sel_hi:[1,0]
	v_rcp_f32_e32 v137, v134
	v_pk_mul_f32 v[132:133], v[132:133], v[140:141]
	v_pk_add_f32 v[142:143], v[142:143], 1.0 op_sel_hi:[1,0]
	v_pk_mul_f32 v[70:71], v[70:71], v[132:133]
	v_cvt_pk_f32_fp8_e32 v[132:133], v135
	v_pk_mul_f32 v[136:137], v[136:137], v[142:143]
	v_cvt_pk_f32_fp8_sdwa v[134:135], v135 src0_sel:WORD_1
	v_pk_mul_f32 v[72:73], v[72:73], v[136:137]
	v_cvt_pk_f32_fp8_e32 v[136:137], v139
	v_add_f32_e32 v132, 1.0, v132
	v_add_f32_e32 v133, 1.0, v133
	v_rcp_f32_e32 v132, v132
	v_rcp_f32_e32 v133, v133
	v_pk_add_f32 v[136:137], v[136:137], 1.0 op_sel_hi:[1,0]
	v_cvt_pk_f32_fp8_sdwa v[138:139], v139 src0_sel:WORD_1
	v_add_f32_e32 v134, 1.0, v134
	v_pk_mul_f32 v[132:133], v[132:133], v[136:137]
	v_add_f32_e32 v135, 1.0, v135
	v_pk_mul_f32 v[66:67], v[66:67], v[132:133]
	v_add_u32_e32 v132, 0xf0000, v130
	global_load_dwordx4 v[140:143], v132, s[64:65] offset:1536 nt
	global_load_dwordx4 v[144:147], v132, s[64:65] offset:2560 nt
	v_add_u32_e32 v132, 0x10e000, v130
	global_load_dwordx4 v[156:159], v132, s[64:65] offset:1536 nt
	global_load_dwordx4 v[160:163], v132, s[64:65] offset:2560 nt
	v_rcp_f32_e32 v134, v134
	v_rcp_f32_e32 v135, v135
	v_pk_add_f32 v[138:139], v[138:139], 1.0 op_sel_hi:[1,0]
	v_add_u32_e32 v132, 0x12c000, v130
	v_add_u32_e32 v130, 0x14a000, v130
	v_pk_mul_f32 v[134:135], v[134:135], v[138:139]
	global_load_dwordx4 v[148:151], v132, s[64:65] offset:1536 nt
	global_load_dwordx4 v[152:155], v132, s[64:65] offset:2560 nt
	v_pk_mul_f32 v[68:69], v[68:69], v[134:135]
	global_load_dwordx4 v[132:135], v130, s[64:65] offset:1536 nt
	global_load_dwordx4 v[136:139], v130, s[64:65] offset:2560 nt
	s_waitcnt vmcnt(0)
	v_cvt_pk_f32_fp8_e32 v[186:187], v140
	v_cvt_pk_f32_fp8_e32 v[190:191], v144
	v_cvt_pk_f32_fp8_sdwa v[188:189], v140 src0_sel:WORD_1
	v_cvt_pk_f32_fp8_sdwa v[192:193], v144 src0_sel:WORD_1
	v_add_f32_e32 v130, 1.0, v186
	v_rcp_f32_e32 v186, v130
	v_add_f32_e32 v130, 1.0, v187
	v_rcp_f32_e32 v187, v130
	v_pk_add_f32 v[190:191], v[190:191], 1.0 op_sel_hi:[1,0]
	v_add_f32_e32 v130, 1.0, v188
	v_rcp_f32_e32 v188, v130
	v_pk_mul_f32 v[186:187], v[186:187], v[190:191]
	v_add_f32_e32 v130, 1.0, v189
	v_pk_mul_f32 v[62:63], v[62:63], v[186:187]
	v_cvt_pk_f32_fp8_e32 v[186:187], v141
	v_rcp_f32_e32 v189, v130
	v_cvt_pk_f32_fp8_sdwa v[140:141], v141 src0_sel:WORD_1
	v_pk_add_f32 v[192:193], v[192:193], 1.0 op_sel_hi:[1,0]
	v_add_f32_e32 v130, 1.0, v186
	v_rcp_f32_e32 v186, v130
	v_add_f32_e32 v130, 1.0, v187
	v_pk_mul_f32 v[188:189], v[188:189], v[192:193]
	v_rcp_f32_e32 v187, v130
	v_add_f32_e32 v130, 1.0, v140
	v_pk_mul_f32 v[64:65], v[64:65], v[188:189]
	v_cvt_pk_f32_fp8_e32 v[188:189], v145
	v_cvt_pk_f32_fp8_sdwa v[144:145], v145 src0_sel:WORD_1
	v_rcp_f32_e32 v140, v130
	v_add_f32_e32 v130, 1.0, v141
	v_rcp_f32_e32 v141, v130
	v_pk_add_f32 v[144:145], v[144:145], 1.0 op_sel_hi:[1,0]
	v_pk_add_f32 v[188:189], v[188:189], 1.0 op_sel_hi:[1,0]
	v_pk_mul_f32 v[140:141], v[140:141], v[144:145]
	s_nop 0
	v_pk_mul_f32 v[60:61], v[60:61], v[140:141]
	v_cvt_pk_f32_fp8_e32 v[140:141], v142
	v_pk_mul_f32 v[186:187], v[186:187], v[188:189]
	v_cvt_pk_f32_fp8_sdwa v[144:145], v142 src0_sel:WORD_1
	v_pk_mul_f32 v[58:59], v[58:59], v[186:187]
	v_add_f32_e32 v130, 1.0, v140
	v_cvt_pk_f32_fp8_e32 v[186:187], v146
	v_rcp_f32_e32 v140, v130
	v_add_f32_e32 v130, 1.0, v141
	v_rcp_f32_e32 v141, v130
	v_add_f32_e32 v130, 1.0, v144
	v_pk_add_f32 v[186:187], v[186:187], 1.0 op_sel_hi:[1,0]
	v_cvt_pk_f32_fp8_sdwa v[188:189], v146 src0_sel:WORD_1
	v_rcp_f32_e32 v144, v130
	v_add_f32_e32 v130, 1.0, v145
	v_pk_mul_f32 v[140:141], v[140:141], v[186:187]
	v_rcp_f32_e32 v145, v130
	v_pk_mul_f32 v[54:55], v[54:55], v[140:141]
	v_cvt_pk_f32_fp8_e32 v[140:141], v143
	v_pk_add_f32 v[188:189], v[188:189], 1.0 op_sel_hi:[1,0]
	v_cvt_pk_f32_fp8_sdwa v[142:143], v143 src0_sel:WORD_1
	v_pk_mul_f32 v[144:145], v[144:145], v[188:189]
	v_add_f32_e32 v130, 1.0, v140
	v_pk_mul_f32 v[56:57], v[56:57], v[144:145]
	v_cvt_pk_f32_fp8_e32 v[144:145], v147
	v_rcp_f32_e32 v140, v130
	v_add_f32_e32 v130, 1.0, v141
	v_rcp_f32_e32 v141, v130
	v_pk_add_f32 v[144:145], v[144:145], 1.0 op_sel_hi:[1,0]
	v_add_f32_e32 v130, 1.0, v142
	v_cvt_pk_f32_fp8_sdwa v[146:147], v147 src0_sel:WORD_1
	v_pk_mul_f32 v[140:141], v[140:141], v[144:145]
	v_rcp_f32_e32 v142, v130
	v_pk_mul_f32 v[50:51], v[50:51], v[140:141]
	v_cvt_pk_f32_fp8_e32 v[140:141], v156
	v_add_f32_e32 v130, 1.0, v143
	v_rcp_f32_e32 v143, v130
	v_pk_add_f32 v[146:147], v[146:147], 1.0 op_sel_hi:[1,0]
	v_add_f32_e32 v130, 1.0, v140
	v_cvt_pk_f32_fp8_e32 v[144:145], v160
	v_rcp_f32_e32 v140, v130
	v_add_f32_e32 v130, 1.0, v141
	v_pk_mul_f32 v[142:143], v[142:143], v[146:147]
	v_rcp_f32_e32 v141, v130
	v_pk_mul_f32 v[52:53], v[52:53], v[142:143]
	v_cvt_pk_f32_fp8_sdwa v[142:143], v156 src0_sel:WORD_1
	v_pk_add_f32 v[144:145], v[144:145], 1.0 op_sel_hi:[1,0]
	v_cvt_pk_f32_fp8_sdwa v[146:147], v160 src0_sel:WORD_1
	v_pk_mul_f32 v[140:141], v[140:141], v[144:145]
	v_add_f32_e32 v130, 1.0, v142
	v_pk_mul_f32 v[46:47], v[46:47], v[140:141]
	v_cvt_pk_f32_fp8_e32 v[140:141], v157
	v_rcp_f32_e32 v142, v130
	v_add_f32_e32 v130, 1.0, v143
	v_rcp_f32_e32 v143, v130
	v_add_f32_e32 v130, 1.0, v140
	v_pk_add_f32 v[146:147], v[146:147], 1.0 op_sel_hi:[1,0]
	v_cvt_pk_f32_fp8_e32 v[144:145], v161
	v_rcp_f32_e32 v140, v130
	v_add_f32_e32 v130, 1.0, v141
	v_pk_mul_f32 v[142:143], v[142:143], v[146:147]
	v_rcp_f32_e32 v141, v130
	v_pk_mul_f32 v[48:49], v[48:49], v[142:143]
	v_cvt_pk_f32_fp8_sdwa v[142:143], v157 src0_sel:WORD_1
	v_pk_add_f32 v[144:145], v[144:145], 1.0 op_sel_hi:[1,0]
	v_cvt_pk_f32_fp8_sdwa v[146:147], v161 src0_sel:WORD_1
	v_pk_mul_f32 v[140:141], v[140:141], v[144:145]
	v_add_f32_e32 v130, 1.0, v142
	v_pk_mul_f32 v[42:43], v[42:43], v[140:141]
	v_cvt_pk_f32_fp8_e32 v[140:141], v158
	v_rcp_f32_e32 v142, v130
	v_add_f32_e32 v130, 1.0, v143
	v_rcp_f32_e32 v143, v130
	v_add_f32_e32 v130, 1.0, v140
	v_pk_add_f32 v[146:147], v[146:147], 1.0 op_sel_hi:[1,0]
	v_cvt_pk_f32_fp8_e32 v[144:145], v162
	v_rcp_f32_e32 v140, v130
	v_add_f32_e32 v130, 1.0, v141
	v_pk_mul_f32 v[142:143], v[142:143], v[146:147]
	v_rcp_f32_e32 v141, v130
	v_pk_mul_f32 v[44:45], v[44:45], v[142:143]
	v_cvt_pk_f32_fp8_sdwa v[142:143], v158 src0_sel:WORD_1
	v_pk_add_f32 v[144:145], v[144:145], 1.0 op_sel_hi:[1,0]
	v_cvt_pk_f32_fp8_sdwa v[146:147], v162 src0_sel:WORD_1
	v_pk_mul_f32 v[140:141], v[140:141], v[144:145]
	v_add_f32_e32 v130, 1.0, v142
	v_pk_mul_f32 v[38:39], v[38:39], v[140:141]
	v_cvt_pk_f32_fp8_e32 v[140:141], v159
	v_rcp_f32_e32 v142, v130
	v_add_f32_e32 v130, 1.0, v143
	v_rcp_f32_e32 v143, v130
	v_add_f32_e32 v130, 1.0, v140
	v_pk_add_f32 v[146:147], v[146:147], 1.0 op_sel_hi:[1,0]
	v_cvt_pk_f32_fp8_e32 v[144:145], v163
	v_rcp_f32_e32 v140, v130
	v_add_f32_e32 v130, 1.0, v141
	v_pk_mul_f32 v[142:143], v[142:143], v[146:147]
	v_rcp_f32_e32 v141, v130
	v_pk_mul_f32 v[40:41], v[40:41], v[142:143]
	v_cvt_pk_f32_fp8_sdwa v[142:143], v159 src0_sel:WORD_1
	v_pk_add_f32 v[144:145], v[144:145], 1.0 op_sel_hi:[1,0]
	v_cvt_pk_f32_fp8_sdwa v[146:147], v163 src0_sel:WORD_1
	v_pk_mul_f32 v[140:141], v[140:141], v[144:145]
	v_add_f32_e32 v130, 1.0, v142
	v_pk_mul_f32 v[34:35], v[34:35], v[140:141]
	v_cvt_pk_f32_fp8_e32 v[140:141], v148
	v_rcp_f32_e32 v142, v130
	v_add_f32_e32 v130, 1.0, v143
	v_rcp_f32_e32 v143, v130
	v_add_f32_e32 v130, 1.0, v140
	v_pk_add_f32 v[146:147], v[146:147], 1.0 op_sel_hi:[1,0]
	v_cvt_pk_f32_fp8_e32 v[144:145], v152
	v_rcp_f32_e32 v140, v130
	v_add_f32_e32 v130, 1.0, v141
	v_pk_mul_f32 v[142:143], v[142:143], v[146:147]
	v_rcp_f32_e32 v141, v130
	v_pk_mul_f32 v[36:37], v[36:37], v[142:143]
	v_cvt_pk_f32_fp8_sdwa v[142:143], v148 src0_sel:WORD_1
	v_pk_add_f32 v[144:145], v[144:145], 1.0 op_sel_hi:[1,0]
	v_cvt_pk_f32_fp8_sdwa v[146:147], v152 src0_sel:WORD_1
	v_pk_mul_f32 v[140:141], v[140:141], v[144:145]
	v_add_f32_e32 v130, 1.0, v142
	v_pk_mul_f32 v[30:31], v[30:31], v[140:141]
	v_cvt_pk_f32_fp8_e32 v[140:141], v149
	v_rcp_f32_e32 v142, v130
	v_add_f32_e32 v130, 1.0, v143
	v_rcp_f32_e32 v143, v130
	v_add_f32_e32 v130, 1.0, v140
	v_pk_add_f32 v[146:147], v[146:147], 1.0 op_sel_hi:[1,0]
	v_cvt_pk_f32_fp8_e32 v[144:145], v153
	v_rcp_f32_e32 v140, v130
	v_add_f32_e32 v130, 1.0, v141
	v_pk_mul_f32 v[142:143], v[142:143], v[146:147]
	v_rcp_f32_e32 v141, v130
	v_pk_mul_f32 v[32:33], v[32:33], v[142:143]
	v_cvt_pk_f32_fp8_sdwa v[142:143], v149 src0_sel:WORD_1
	v_pk_add_f32 v[144:145], v[144:145], 1.0 op_sel_hi:[1,0]
	v_cvt_pk_f32_fp8_sdwa v[146:147], v153 src0_sel:WORD_1
	v_pk_mul_f32 v[140:141], v[140:141], v[144:145]
	v_add_f32_e32 v130, 1.0, v142
	v_pk_mul_f32 v[26:27], v[26:27], v[140:141]
	v_cvt_pk_f32_fp8_e32 v[140:141], v150
	v_rcp_f32_e32 v142, v130
	v_add_f32_e32 v130, 1.0, v143
	v_rcp_f32_e32 v143, v130
	v_add_f32_e32 v130, 1.0, v140
	v_pk_add_f32 v[146:147], v[146:147], 1.0 op_sel_hi:[1,0]
	v_cvt_pk_f32_fp8_e32 v[144:145], v154
	v_rcp_f32_e32 v140, v130
	v_add_f32_e32 v130, 1.0, v141
	v_pk_mul_f32 v[142:143], v[142:143], v[146:147]
	v_rcp_f32_e32 v141, v130
	v_pk_mul_f32 v[28:29], v[28:29], v[142:143]
	v_cvt_pk_f32_fp8_sdwa v[142:143], v150 src0_sel:WORD_1
	v_pk_add_f32 v[144:145], v[144:145], 1.0 op_sel_hi:[1,0]
	v_cvt_pk_f32_fp8_sdwa v[146:147], v154 src0_sel:WORD_1
	v_pk_mul_f32 v[140:141], v[140:141], v[144:145]
	v_add_f32_e32 v130, 1.0, v142
	v_pk_mul_f32 v[22:23], v[22:23], v[140:141]
	v_cvt_pk_f32_fp8_e32 v[140:141], v151
	v_rcp_f32_e32 v142, v130
	v_add_f32_e32 v130, 1.0, v143
	v_rcp_f32_e32 v143, v130
	v_add_f32_e32 v130, 1.0, v140
	v_pk_add_f32 v[146:147], v[146:147], 1.0 op_sel_hi:[1,0]
	v_cvt_pk_f32_fp8_e32 v[144:145], v155
	v_rcp_f32_e32 v140, v130
	v_add_f32_e32 v130, 1.0, v141
	v_pk_mul_f32 v[142:143], v[142:143], v[146:147]
	v_rcp_f32_e32 v141, v130
	v_pk_mul_f32 v[24:25], v[24:25], v[142:143]
	v_cvt_pk_f32_fp8_sdwa v[142:143], v151 src0_sel:WORD_1
	v_pk_add_f32 v[144:145], v[144:145], 1.0 op_sel_hi:[1,0]
	v_cvt_pk_f32_fp8_sdwa v[146:147], v155 src0_sel:WORD_1
	v_pk_mul_f32 v[140:141], v[140:141], v[144:145]
	v_add_f32_e32 v130, 1.0, v142
	v_pk_mul_f32 v[18:19], v[18:19], v[140:141]
	v_cvt_pk_f32_fp8_e32 v[140:141], v132
	v_rcp_f32_e32 v142, v130
	v_add_f32_e32 v130, 1.0, v143
	v_rcp_f32_e32 v143, v130
	v_add_f32_e32 v130, 1.0, v140
	v_pk_add_f32 v[146:147], v[146:147], 1.0 op_sel_hi:[1,0]
	v_cvt_pk_f32_fp8_e32 v[144:145], v136
	v_rcp_f32_e32 v140, v130
	v_add_f32_e32 v130, 1.0, v141
	v_pk_mul_f32 v[142:143], v[142:143], v[146:147]
	v_rcp_f32_e32 v141, v130
	v_pk_mul_f32 v[20:21], v[20:21], v[142:143]
	v_cvt_pk_f32_fp8_sdwa v[142:143], v132 src0_sel:WORD_1
	v_pk_add_f32 v[144:145], v[144:145], 1.0 op_sel_hi:[1,0]
	v_cvt_pk_f32_fp8_sdwa v[146:147], v136 src0_sel:WORD_1
	v_pk_mul_f32 v[140:141], v[140:141], v[144:145]
	v_add_f32_e32 v130, 1.0, v142
	v_pk_mul_f32 v[14:15], v[14:15], v[140:141]
	v_cvt_pk_f32_fp8_e32 v[140:141], v133
	v_rcp_f32_e32 v142, v130
	v_add_f32_e32 v130, 1.0, v143
	v_rcp_f32_e32 v143, v130
	v_cvt_pk_f32_fp8_sdwa v[132:133], v133 src0_sel:WORD_1
	v_add_f32_e32 v130, 1.0, v140
	v_pk_add_f32 v[146:147], v[146:147], 1.0 op_sel_hi:[1,0]
	v_rcp_f32_e32 v140, v130
	v_add_f32_e32 v130, 1.0, v141
	v_pk_mul_f32 v[142:143], v[142:143], v[146:147]
	v_rcp_f32_e32 v141, v130
	v_add_f32_e32 v130, 1.0, v132
	v_pk_mul_f32 v[16:17], v[16:17], v[142:143]
	v_cvt_pk_f32_fp8_e32 v[142:143], v137
	v_cvt_pk_f32_fp8_sdwa v[136:137], v137 src0_sel:WORD_1
	v_rcp_f32_e32 v132, v130
	v_add_f32_e32 v130, 1.0, v133
	v_rcp_f32_e32 v133, v130
	v_pk_add_f32 v[136:137], v[136:137], 1.0 op_sel_hi:[1,0]
	v_pk_add_f32 v[142:143], v[142:143], 1.0 op_sel_hi:[1,0]
	v_pk_mul_f32 v[132:133], v[132:133], v[136:137]
	s_nop 0
	v_pk_mul_f32 v[12:13], v[12:13], v[132:133]
	v_cvt_pk_f32_fp8_e32 v[132:133], v134
	v_pk_mul_f32 v[140:141], v[140:141], v[142:143]
	v_cvt_pk_f32_fp8_sdwa v[136:137], v134 src0_sel:WORD_1
	v_pk_mul_f32 v[10:11], v[10:11], v[140:141]
	v_add_f32_e32 v130, 1.0, v132
	v_cvt_pk_f32_fp8_e32 v[140:141], v138
	v_rcp_f32_e32 v132, v130
	v_add_f32_e32 v130, 1.0, v133
	v_rcp_f32_e32 v133, v130
	v_pk_add_f32 v[140:141], v[140:141], 1.0 op_sel_hi:[1,0]
	v_add_f32_e32 v130, 1.0, v136
	v_cvt_pk_f32_fp8_sdwa v[142:143], v138 src0_sel:WORD_1
	v_pk_mul_f32 v[132:133], v[132:133], v[140:141]
	v_rcp_f32_e32 v136, v130
	v_pk_mul_f32 v[6:7], v[6:7], v[132:133]
	v_cvt_pk_f32_fp8_e32 v[132:133], v135
	v_add_f32_e32 v130, 1.0, v137
	v_rcp_f32_e32 v137, v130
	v_cvt_pk_f32_fp8_sdwa v[134:135], v135 src0_sel:WORD_1
	v_add_f32_e32 v130, 1.0, v132
	v_pk_add_f32 v[142:143], v[142:143], 1.0 op_sel_hi:[1,0]
	v_rcp_f32_e32 v132, v130
	v_add_f32_e32 v130, 1.0, v133
	v_pk_mul_f32 v[136:137], v[136:137], v[142:143]
	v_rcp_f32_e32 v133, v130
	v_add_f32_e32 v130, 1.0, v134
	v_pk_mul_f32 v[8:9], v[8:9], v[136:137]
	v_cvt_pk_f32_fp8_e32 v[136:137], v139
	v_cvt_pk_f32_fp8_sdwa v[138:139], v139 src0_sel:WORD_1
	v_rcp_f32_e32 v134, v130
	v_add_f32_e32 v130, 1.0, v135
	v_rcp_f32_e32 v135, v130
	v_pk_add_f32 v[138:139], v[138:139], 1.0 op_sel_hi:[1,0]
	v_pk_add_f32 v[136:137], v[136:137], 1.0 op_sel_hi:[1,0]
	v_pk_mul_f32 v[134:135], v[134:135], v[138:139]
	v_pk_mul_f32 v[132:133], v[132:133], v[136:137]
	v_pk_mul_f32 v[4:5], v[4:5], v[134:135]
	v_pk_mul_f32 v[2:3], v[2:3], v[132:133]
	s_branch .LBB0_1103

.LBB0_1555:
	s_or_b64 exec, exec, s[8:9]
	s_lshl_b32 s22, s17, 11
	s_addk_i32 s22, 0x800
	s_min_i32 s23, s22, s0
	v_add_u32_e32 v29, s16, v23
	s_lshl_b32 s24, s17, 8
	v_cmp_gt_i32_e64 s[8:9], s23, v29
	s_waitcnt vmcnt(0)
	ds_write_b128 v67, v[0:3]
	s_waitcnt lgkmcnt(0)
	s_barrier
	s_and_saveexec_b64 s[10:11], s[8:9]
	s_cbranch_execz .LBB0_1557
	v_add_u32_e32 v0, s24, v29
	v_ashrrev_i32_e32 v1, 31, v0
	v_lshlrev_b64 v[2:3], 11, v[0:1]
	v_lshl_add_u64 v[2:3], v[20:21], 0, v[2:3]
	v_lshlrev_b64 v[0:1], 6, v[0:1]
	global_load_dwordx2 v[50:51], v[2:3], off nt
	global_load_dwordx2 v[52:53], v[2:3], off offset:512 nt
	global_load_dwordx2 v[56:57], v[2:3], off offset:1024 nt
	global_load_dwordx2 v[58:59], v[2:3], off offset:1536 nt
	v_lshl_or_b32 v0, v22, 2, v0
	v_lshl_add_u64 v[2:3], s[14:15], 0, v[0:1]
	v_lshl_add_u64 v[0:1], s[12:13], 0, v[0:1]
	global_load_dword v71, v[2:3], off nt
	global_load_dword v72, v[0:1], off nt

.LBB0_1559:
	s_or_b64 exec, exec, s[20:21]
	v_and_b32_e32 v85, 0xffff0000, v46
	v_and_b32_e32 v87, 0xffff0000, v47
	v_and_b32_e32 v89, 0xffff0000, v44
	v_and_b32_e32 v91, 0xffff0000, v45
	v_lshlrev_b32_e32 v84, 16, v46
	v_lshlrev_b32_e32 v86, 16, v47
	v_lshlrev_b32_e32 v88, 16, v44
	v_lshlrev_b32_e32 v90, 16, v45
	ds_read_b128 v[44:47], v61 offset:4096
	v_and_b32_e32 v55, 0xffff0000, v48
	v_and_b32_e32 v83, 0xffff0000, v49
	v_lshlrev_b32_e32 v54, 16, v48
	v_lshlrev_b32_e32 v82, 16, v49
	ds_read_b128 v[74:77], v61
	ds_read_b128 v[78:81], v61 offset:5120
	v_and_b32_e32 v93, 0xffff0000, v42
	v_and_b32_e32 v95, 0xffff0000, v43
	v_lshlrev_b32_e32 v92, 16, v42
	v_lshlrev_b32_e32 v94, 16, v43
	s_waitcnt lgkmcnt(2)
	v_pk_fma_f32 v[42:43], v[14:15], v[46:47], v[82:83]
	v_pk_fma_f32 v[44:45], v[12:13], v[44:45], v[54:55]
	ds_read_b128 v[12:15], v61 offset:1024
	v_lshlrev_b32_e32 v46, 16, v40
	v_and_b32_e32 v47, 0xffff0000, v40
	v_lshlrev_b32_e32 v40, 16, v41
	v_and_b32_e32 v41, 0xffff0000, v41
	s_waitcnt lgkmcnt(2)
	v_pk_fma_f32 v[42:43], v[76:77], v[40:41], v[42:43]
	s_waitcnt lgkmcnt(1)
	v_pk_fma_f32 v[40:41], v[10:11], v[80:81], v[86:87]
	v_pk_fma_f32 v[8:9], v[8:9], v[78:79], v[84:85]
	v_lshlrev_b32_e32 v10, 16, v38
	v_and_b32_e32 v11, 0xffff0000, v38
	v_pk_fma_f32 v[44:45], v[74:75], v[46:47], v[44:45]
	s_waitcnt lgkmcnt(0)
	v_pk_fma_f32 v[46:47], v[12:13], v[10:11], v[8:9]
	ds_read_b128 v[8:11], v61 offset:6144
	v_lshlrev_b32_e32 v12, 16, v39
	v_and_b32_e32 v13, 0xffff0000, v39
	v_pk_fma_f32 v[48:49], v[14:15], v[12:13], v[40:41]
	ds_read_b128 v[12:15], v61 offset:2048
	ds_read_b128 v[38:41], v61 offset:7168
	s_waitcnt lgkmcnt(2)
	v_pk_fma_f32 v[10:11], v[6:7], v[10:11], v[90:91]
	v_pk_fma_f32 v[8:9], v[4:5], v[8:9], v[88:89]
	ds_read_b128 v[4:7], v61 offset:3072
	v_lshlrev_b32_e32 v54, 16, v36
	v_and_b32_e32 v55, 0xffff0000, v36
	s_waitcnt lgkmcnt(2)
	v_pk_fma_f32 v[8:9], v[12:13], v[54:55], v[8:9]
	v_lshlrev_b32_e32 v12, 16, v37
	v_and_b32_e32 v13, 0xffff0000, v37
	v_pk_fma_f32 v[10:11], v[14:15], v[12:13], v[10:11]
	s_waitcnt lgkmcnt(1)
	v_pk_fma_f32 v[0:1], v[0:1], v[38:39], v[92:93]
	v_lshlrev_b32_e32 v12, 16, v34
	v_and_b32_e32 v13, 0xffff0000, v34
	v_pk_fma_f32 v[2:3], v[2:3], v[40:41], v[94:95]
	s_waitcnt lgkmcnt(0)
	v_pk_fma_f32 v[12:13], v[4:5], v[12:13], v[0:1]
	v_lshlrev_b32_e32 v0, 16, v35
	v_and_b32_e32 v1, 0xffff0000, v35
	v_pk_fma_f32 v[14:15], v[6:7], v[0:1], v[2:3]
	v_mov_b32_e32 v2, v45
	v_mov_b32_e32 v3, v47
	v_mov_b32_e32 v0, v44
	v_mov_b32_e32 v1, v46
	v_pk_mul_f32 v[2:3], v[2:3], v[2:3]
	v_mov_b32_e32 v4, v9
	v_pk_fma_f32 v[0:1], v[0:1], v[0:1], v[2:3]
	v_mov_b32_e32 v2, v42
	v_mov_b32_e32 v3, v48
	v_pk_fma_f32 v[0:1], v[2:3], v[2:3], v[0:1]
	v_mov_b32_e32 v2, v43
	v_mov_b32_e32 v3, v49
	v_mov_b32_e32 v5, v13
	v_pk_fma_f32 v[0:1], v[2:3], v[2:3], v[0:1]
	v_mov_b32_e32 v2, v8
	v_mov_b32_e32 v3, v12
	v_pk_mul_f32 v[4:5], v[4:5], v[4:5]
	v_add_f32_e32 v0, v0, v1
	v_pk_fma_f32 v[2:3], v[2:3], v[2:3], v[4:5]
	v_mov_b32_e32 v4, v10
	v_mov_b32_e32 v5, v14
	v_pk_fma_f32 v[2:3], v[4:5], v[4:5], v[2:3]
	v_mov_b32_e32 v4, v11
	v_mov_b32_e32 v5, v15
	v_pk_fma_f32 v[2:3], v[4:5], v[4:5], v[2:3]
	v_and_b32_e32 v1, 64, v177
	v_add_f32_e32 v0, v0, v2
	v_add_u32_e32 v1, 64, v1
	v_xor_b32_e32 v2, 32, v177
	v_cmp_lt_i32_e64 s[10:11], v2, v1
	v_add_f32_e32 v0, v0, v3
	s_and_b64 s[8:9], exec, s[8:9]
	v_cndmask_b32_e64 v2, v177, v2, s[10:11]
	v_lshlrev_b32_e32 v2, 2, v2
	ds_bpermute_b32 v2, v2, v0
	s_or_b64 s[18:19], s[8:9], s[18:19]
	s_load_dwordx2 s[8:9], s[96:97], 0xd8
	v_ashrrev_i32_e32 v33, 31, v32
	s_waitcnt lgkmcnt(0)
	v_add_f32_e32 v0, v0, v2
	v_xor_b32_e32 v2, 16, v177
	v_cmp_lt_i32_e64 s[10:11], v2, v1
	s_nop 1
	v_cndmask_b32_e64 v2, v177, v2, s[10:11]
	v_lshlrev_b32_e32 v2, 2, v2
	ds_bpermute_b32 v2, v2, v0
	s_waitcnt lgkmcnt(0)
	v_add_f32_e32 v0, v0, v2
	v_xor_b32_e32 v2, 8, v177
	v_cmp_lt_i32_e64 s[10:11], v2, v1
	s_nop 1
	v_cndmask_b32_e64 v2, v177, v2, s[10:11]
	v_lshlrev_b32_e32 v2, 2, v2
	ds_bpermute_b32 v2, v2, v0
	s_waitcnt lgkmcnt(0)
	v_add_f32_e32 v0, v0, v2
	v_xor_b32_e32 v2, 4, v177
	v_cmp_lt_i32_e64 s[10:11], v2, v1
	s_nop 1
	v_cndmask_b32_e64 v2, v177, v2, s[10:11]
	v_lshlrev_b32_e32 v2, 2, v2
	ds_bpermute_b32 v2, v2, v0
	s_waitcnt lgkmcnt(0)
	v_add_f32_e32 v0, v0, v2
	v_xor_b32_e32 v2, 2, v177
	v_cmp_lt_i32_e64 s[10:11], v2, v1
	s_nop 1
	v_cndmask_b32_e64 v2, v177, v2, s[10:11]
	v_lshlrev_b32_e32 v2, 2, v2
	ds_bpermute_b32 v2, v2, v0
	s_waitcnt lgkmcnt(0)
	v_add_f32_e32 v0, v0, v2
	v_xor_b32_e32 v2, 1, v177
	v_cmp_lt_i32_e64 s[10:11], v2, v1
	s_nop 1
	v_cndmask_b32_e64 v1, v177, v2, s[10:11]
	v_lshlrev_b32_e32 v1, 2, v1
	ds_bpermute_b32 v1, v1, v0
	s_waitcnt lgkmcnt(0)
	v_add_f32_e32 v0, v0, v1
	v_fmamk_f32 v0, v0, 0x3a800000, v68
	v_mul_f32_e32 v1, 0x4b800000, v0
	v_cmp_gt_f32_e64 s[10:11], s1, v0
	s_nop 1
	v_cndmask_b32_e64 v0, v0, v1, s[10:11]
	v_rsq_f32_e32 v0, v0
	s_nop 0
	v_mul_f32_e32 v1, 0x45800000, v0
	v_cndmask_b32_e64 v34, v0, v1, s[10:11]
	v_lshlrev_b64 v[0:1], 12, v[32:33]
	v_lshl_add_u64 v[4:5], s[8:9], 0, v[0:1]
	ds_read_b128 v[0:3], v61 offset:8192
	v_lshl_add_u64 v[32:33], v[4:5], 0, v[16:17]
	ds_read_b128 v[4:7], v61 offset:9216
	v_pk_mul_f32 v[36:37], v[44:45], v[34:35] op_sel_hi:[1,0]
	v_pk_mul_f32 v[38:39], v[42:43], v[34:35] op_sel_hi:[1,0]
	s_waitcnt lgkmcnt(1)
	v_pk_mul_f32 v[0:1], v[0:1], v[36:37]
	v_pk_mul_f32 v[2:3], v[2:3], v[38:39]
	global_store_dwordx4 v[32:33], v[0:3], off nt
	v_pk_mul_f32 v[8:9], v[8:9], v[34:35] op_sel_hi:[1,0]
	v_pk_mul_f32 v[10:11], v[10:11], v[34:35] op_sel_hi:[1,0]
	v_pk_mul_f32 v[0:1], v[46:47], v[34:35] op_sel_hi:[1,0]
	v_pk_mul_f32 v[2:3], v[48:49], v[34:35] op_sel_hi:[1,0]
	s_waitcnt lgkmcnt(0)
	v_pk_mul_f32 v[0:1], v[4:5], v[0:1]
	v_pk_mul_f32 v[2:3], v[6:7], v[2:3]
	ds_read_b128 v[4:7], v61 offset:10240
	global_store_dwordx4 v[32:33], v[0:3], off offset:1024 nt
	ds_read_b128 v[0:3], v61 offset:11264
	s_waitcnt lgkmcnt(1)
	v_pk_mul_f32 v[6:7], v[6:7], v[10:11]
	v_pk_mul_f32 v[4:5], v[4:5], v[8:9]
	global_store_dwordx4 v[32:33], v[4:7], off offset:2048 nt
	s_nop 1
	v_pk_mul_f32 v[4:5], v[12:13], v[34:35] op_sel_hi:[1,0]
	v_pk_mul_f32 v[6:7], v[14:15], v[34:35] op_sel_hi:[1,0]
	s_waitcnt lgkmcnt(0)
	v_pk_mul_f32 v[0:1], v[0:1], v[4:5]
	v_pk_mul_f32 v[2:3], v[2:3], v[6:7]
	global_store_dwordx4 v[32:33], v[0:3], off offset:3072 nt
	s_andn2_b64 exec, exec, s[18:19]
	s_cbranch_execz .LBB0_1541
.LBB0_1560:
	v_mov_b32_e32 v32, v29
	v_add_u32_e32 v54, s24, v32
	v_ashrrev_i32_e32 v55, 31, v54
	v_lshlrev_b64 v[0:1], 11, v[54:55]
	v_lshl_add_u64 v[0:1], v[24:25], 0, v[0:1]
	global_load_dwordx2 v[40:41], v[0:1], off nt
	global_load_dwordx2 v[38:39], v[0:1], off offset:512 nt
	global_load_dwordx2 v[36:37], v[0:1], off offset:1024 nt
	global_load_dwordx2 v[34:35], v[0:1], off offset:1536 nt
	s_waitcnt vmcnt(5)
	v_cmp_lt_i32_e64 s[8:9], -1, v71
	v_mov_b32_e32 v12, 0
	v_mov_b64_e32 v[42:43], v[58:59]
	v_mov_b64_e32 v[44:45], v[56:57]
	v_mov_b64_e32 v[46:47], v[52:53]
	v_mov_b64_e32 v[48:49], v[50:51]
	s_and_b32 s8, s8, 0xffff
	v_mov_b32_e32 v13, v12
	v_mov_b32_e32 v14, v12
	v_mov_b32_e32 v15, v12
	v_mov_b32_e32 v8, v12
	v_mov_b32_e32 v9, v12
	v_mov_b32_e32 v10, v12
	v_mov_b32_e32 v11, v12
	v_mov_b32_e32 v4, v12
	v_mov_b32_e32 v5, v12
	v_mov_b32_e32 v6, v12
	v_mov_b32_e32 v7, v12
	v_mov_b32_e32 v0, v12
	v_mov_b32_e32 v1, v12
	v_mov_b32_e32 v2, v12
	v_mov_b32_e32 v3, v12
	s_branch .LBB0_1563
.LBB0_1561:
	s_ff1_i32_b32 s11, s10
	v_readlane_b32 s8, v71, s11
	s_add_i32 s20, s10, -1
	s_mul_i32 s9, s11, 0x1200
	s_ashr_i32 s21, s8, 31
	s_add_u32 s8, s8, s9
	s_addc_u32 s9, s21, 0
	s_lshl_b64 s[8:9], s[8:9], 10
	v_lshl_add_u64 v[98:99], v[26:27], 0, s[8:9]
	global_load_dword v96, v[98:99], off nt
	global_load_dword v95, v[98:99], off offset:256 nt
	global_load_dword v91, v[98:99], off offset:512 nt
	global_load_dword v89, v[98:99], off offset:768 nt
	s_waitcnt vmcnt(8)
	v_readlane_b32 s8, v72, s11
	s_nop 1
	v_mul_f32_e32 v66, s8, v70
	s_and_b32 s8, s20, s10

.LBB0_1563:
	s_cmp_eq_u32 s8, 0
	s_mov_b32 s9, 0
	v_mov_b32_e32 v29, 0
	v_mov_b32_e32 v31, 0
	v_mov_b32_e32 v33, 0
	v_mov_b32_e32 v51, 0
	v_mov_b32_e32 v50, 0
	s_mov_b32 s10, 0
	s_cbranch_scc1 .LBB0_1565
	s_ff1_i32_b32 s20, s8
	v_readlane_b32 s10, v71, s20
	s_add_i32 s21, s8, -1
	s_mul_i32 s11, s20, 0x1200
	s_ashr_i32 s25, s10, 31
	s_add_u32 s10, s10, s11
	s_addc_u32 s11, s25, 0
	s_lshl_b64 s[10:11], s[10:11], 10
	v_lshl_add_u64 v[52:53], v[26:27], 0, s[10:11]
	global_load_dword v51, v[52:53], off nt
	global_load_dword v33, v[52:53], off offset:256 nt
	global_load_dword v31, v[52:53], off offset:512 nt
	global_load_dword v29, v[52:53], off offset:768 nt
	s_waitcnt vmcnt(8)
	v_readlane_b32 s10, v72, s20
	s_nop 1
	v_mul_f32_e32 v50, s10, v70
	s_and_b32 s10, s21, s8
.LBB0_1565:
	v_mov_b32_e32 v55, 0
	s_cmp_eq_u32 s10, 0
	v_mov_b32_e32 v53, 0
	v_mov_b32_e32 v57, 0
	v_mov_b32_e32 v59, 0
	v_mov_b32_e32 v73, 0
	v_mov_b32_e32 v52, 0
	s_cbranch_scc1 .LBB0_1567
	s_ff1_i32_b32 s11, s10
	v_readlane_b32 s8, v71, s11
	s_add_i32 s20, s10, -1
	s_mul_i32 s9, s11, 0x1200
	s_ashr_i32 s21, s8, 31
	s_add_u32 s8, s8, s9
	s_addc_u32 s9, s21, 0
	s_lshl_b64 s[8:9], s[8:9], 10
	v_lshl_add_u64 v[74:75], v[26:27], 0, s[8:9]
	global_load_dword v73, v[74:75], off nt
	global_load_dword v59, v[74:75], off offset:256 nt
	global_load_dword v57, v[74:75], off offset:512 nt
	global_load_dword v55, v[74:75], off offset:768 nt
	s_waitcnt vmcnt(8)
	v_readlane_b32 s8, v72, s11
	s_and_b32 s9, s20, s10
	s_nop 0
	v_mul_f32_e32 v52, s8, v70
.LBB0_1567:
	s_cmp_eq_u32 s9, 0
	s_mov_b32 s8, 0
	v_mov_b32_e32 v74, 0
	v_mov_b32_e32 v75, 0
	v_mov_b32_e32 v76, 0
	v_mov_b32_e32 v56, 0
	s_mov_b32 s10, 0
	s_cbranch_scc1 .LBB0_1569
	s_ff1_i32_b32 s20, s9
	v_readlane_b32 s10, v71, s20
	s_add_i32 s21, s9, -1
	s_mul_i32 s11, s20, 0x1200
	s_ashr_i32 s25, s10, 31
	s_add_u32 s10, s10, s11
	s_addc_u32 s11, s25, 0
	s_lshl_b64 s[10:11], s[10:11], 10
	v_lshl_add_u64 v[78:79], v[26:27], 0, s[10:11]
	global_load_dword v76, v[78:79], off nt
	global_load_dword v75, v[78:79], off offset:256 nt
	global_load_dword v74, v[78:79], off offset:512 nt
	global_load_dword v53, v[78:79], off offset:768 nt
	s_waitcnt vmcnt(8)
	v_readlane_b32 s10, v72, s20
	s_nop 1
	v_mul_f32_e32 v56, s10, v70
	s_and_b32 s10, s21, s9
.LBB0_1569:
	v_mov_b32_e32 v78, 0
	s_cmp_eq_u32 s10, 0
	v_mov_b32_e32 v77, 0
	v_mov_b32_e32 v79, 0
	v_mov_b32_e32 v80, 0
	v_mov_b32_e32 v81, 0
	v_mov_b32_e32 v58, 0
	s_cbranch_scc1 .LBB0_1571
	s_ff1_i32_b32 s11, s10
	v_readlane_b32 s8, v71, s11
	s_add_i32 s20, s10, -1
	s_mul_i32 s9, s11, 0x1200
	s_ashr_i32 s21, s8, 31
	s_add_u32 s8, s8, s9
	s_addc_u32 s9, s21, 0
	s_lshl_b64 s[8:9], s[8:9], 10
	v_lshl_add_u64 v[82:83], v[26:27], 0, s[8:9]
	global_load_dword v81, v[82:83], off nt
	global_load_dword v80, v[82:83], off offset:256 nt
	global_load_dword v79, v[82:83], off offset:512 nt
	global_load_dword v78, v[82:83], off offset:768 nt
	s_waitcnt vmcnt(8)
	v_readlane_b32 s8, v72, s11
	s_nop 1
	v_mul_f32_e32 v58, s8, v70
	s_and_b32 s8, s20, s10
.LBB0_1571:
	s_cmp_eq_u32 s8, 0
	s_mov_b32 s9, 0
	v_mov_b32_e32 v82, 0
	v_mov_b32_e32 v83, 0
	v_mov_b32_e32 v84, 0
	v_mov_b32_e32 v60, 0
	s_mov_b32 s10, 0
	s_cbranch_scc1 .LBB0_1573
	s_ff1_i32_b32 s20, s8
	v_readlane_b32 s10, v71, s20
	s_add_i32 s21, s8, -1
	s_mul_i32 s11, s20, 0x1200
	s_ashr_i32 s25, s10, 31
	s_add_u32 s10, s10, s11
	s_addc_u32 s11, s25, 0
	s_lshl_b64 s[10:11], s[10:11], 10
	v_lshl_add_u64 v[86:87], v[26:27], 0, s[10:11]
	global_load_dword v84, v[86:87], off nt
	global_load_dword v83, v[86:87], off offset:256 nt
	global_load_dword v82, v[86:87], off offset:512 nt
	global_load_dword v77, v[86:87], off offset:768 nt
	s_waitcnt vmcnt(8)
	v_readlane_b32 s10, v72, s20
	s_nop 1
	v_mul_f32_e32 v60, s10, v70
	s_and_b32 s10, s21, s8
.LBB0_1573:
	v_mov_b32_e32 v86, 0
	s_cmp_eq_u32 s10, 0
	v_mov_b32_e32 v85, 0
	v_mov_b32_e32 v87, 0
	v_mov_b32_e32 v88, 0
	v_mov_b32_e32 v90, 0
	v_mov_b32_e32 v62, 0
	s_cbranch_scc1 .LBB0_1575
	s_ff1_i32_b32 s11, s10
	v_readlane_b32 s8, v71, s11
	s_add_i32 s20, s10, -1
	s_mul_i32 s9, s11, 0x1200
	s_ashr_i32 s21, s8, 31
	s_add_u32 s8, s8, s9
	s_addc_u32 s9, s21, 0
	s_lshl_b64 s[8:9], s[8:9], 10
	v_lshl_add_u64 v[92:93], v[26:27], 0, s[8:9]
	global_load_dword v90, v[92:93], off nt
	global_load_dword v88, v[92:93], off offset:256 nt
	global_load_dword v87, v[92:93], off offset:512 nt
	global_load_dword v86, v[92:93], off offset:768 nt
	s_waitcnt vmcnt(8)
	v_readlane_b32 s8, v72, s11
	s_and_b32 s9, s20, s10
	s_nop 0
	v_mul_f32_e32 v62, s8, v70
.LBB0_1575:
	s_cmp_eq_u32 s9, 0
	s_mov_b32 s8, 0
	v_mov_b32_e32 v92, 0
	v_mov_b32_e32 v93, 0
	v_mov_b32_e32 v94, 0
	v_mov_b32_e32 v64, 0
	s_mov_b32 s10, 0
	s_cbranch_scc1 .LBB0_1577
	s_ff1_i32_b32 s20, s9
	v_readlane_b32 s10, v71, s20
	s_add_i32 s21, s9, -1
	s_mul_i32 s11, s20, 0x1200
	s_ashr_i32 s25, s10, 31
	s_add_u32 s10, s10, s11
	s_addc_u32 s11, s25, 0
	s_lshl_b64 s[10:11], s[10:11], 10
	v_lshl_add_u64 v[96:97], v[26:27], 0, s[10:11]
	global_load_dword v94, v[96:97], off nt
	global_load_dword v93, v[96:97], off offset:256 nt
	global_load_dword v92, v[96:97], off offset:512 nt
	global_load_dword v85, v[96:97], off offset:768 nt
	s_waitcnt vmcnt(8)
	v_readlane_b32 s10, v72, s20
	s_nop 1
	v_mul_f32_e32 v64, s10, v70
	s_and_b32 s10, s21, s9

.LBB0_1579:
	v_add_u32_e32 v29, 8, v32
	v_cmp_gt_i32_e64 s[10:11], s23, v29
	v_cmp_le_i32_e64 s[8:9], s23, v29
	v_mov_b64_e32 v[50:51], v[48:49]
	v_mov_b64_e32 v[52:53], v[46:47]
	v_mov_b64_e32 v[56:57], v[44:45]
	v_mov_b64_e32 v[58:59], v[42:43]
	s_and_saveexec_b64 s[20:21], s[10:11]
	s_cbranch_execz .LBB0_1559
	v_add_u32_e32 v54, 8, v54
	v_ashrrev_i32_e32 v55, 31, v54
	v_lshlrev_b64 v[50:51], 11, v[54:55]
	v_lshl_add_u64 v[72:73], v[20:21], 0, v[50:51]
	v_lshlrev_b64 v[54:55], 6, v[54:55]
	global_load_dwordx2 v[50:51], v[72:73], off nt
	global_load_dwordx2 v[52:53], v[72:73], off offset:512 nt
	global_load_dwordx2 v[56:57], v[72:73], off offset:1024 nt
	global_load_dwordx2 v[58:59], v[72:73], off offset:1536 nt
	v_lshl_or_b32 v54, v22, 2, v54
	v_lshl_add_u64 v[74:75], s[14:15], 0, v[54:55]
	v_lshl_add_u64 v[54:55], s[12:13], 0, v[54:55]
	global_load_dword v71, v[74:75], off nt
	global_load_dword v72, v[54:55], off nt
	s_branch .LBB0_1559
